# E1/E2: expert ids of a token fetched once per wave by LDS-DMA (16 lanes) instead of replicated global loads
# speedup vs baseline: 1.0008x; 1.0008x over previous
.Le1w_first:
	s_mov_b64 exec, 1
	global_atomic_add v250, v211, v1, s[0:1] sc0
	s_mov_b64 exec, -1
	v_mov_b32_e32 v249, 0x80
	v_and_b32_e32 v233, 7, v0
	v_bfe_u32 v234, v0, 4, 2
	v_xor_b32_e32 v235, v233, v234
	v_lshlrev_b32_e32 v144, 4, v235
	v_xor_b32_e32 v145, 64, v144
	v_and_b32_e32 v233, 15, v0
	v_bfe_u32 v234, v0, 4, 2
	v_bfe_u32 v235, v0, 1, 3
	v_xor_b32_e32 v235, v234, v235
	v_lshlrev_b32_e32 v235, 4, v235
	v_lshl_add_u32 v235, v233, 7, v235
	v_lshrrev_b32_e32 v236, 6, v0
	s_nop 0
	v_readfirstlane_b32 s38, v236
	s_lshl_b32 s38, s38, 14
	v_add_u32_e32 v146, s38, v235
	v_xor_b32_e32 v147, 64, v146
	s_lshr_b32 s99, s38, 4
	s_add_i32 s99, s99, 0x21000
	v_bfe_u32 v234, v0, 4, 2
	v_lshl_add_u32 v148, v234, 6, s99
	s_lshr_b32 s99, s38, 5
	s_add_i32 s99, s99, 0x23000
	v_bfe_u32 v234, v0, 3, 3
	v_lshl_add_u32 v152, v234, 5, s99
	s_add_u32 s2, s96, 0x4c00000
	s_addc_u32 s3, s97, 0
	s_add_u32 s4, s96, 0x27600000
	s_addc_u32 s5, s97, 0
	s_add_u32 s4, s4, s80
	s_addc_u32 s5, s5, 0
	s_lshl_b32 s33, s60, 3
	s_waitcnt vmcnt(0)
	v_readfirstlane_b32 s35, v250
	s_cmp_ge_i32 s35, s33
	s_cbranch_scc1 .LBB0_722
	s_lshr_b32 s99, s35, 3
	s_lshl_b32 s98, s99, 6
	s_and_b32 s99, s99, 0xffffff00
	s_add_i32 s99, s99, 0x100
	s_and_b64 s[24:25], s[30:31], exec
	s_cselect_b32 s99, 0, s99
	s_add_i32 s98, s98, s99
	s_and_b32 s99, s35, 7
	s_lshl_b32 s99, s99, 3
	s_add_i32 s98, s98, s99
	s_mov_b32 s39, s98
	v_and_b32_e32 v234, 15, v0
	s_lshl_b32 s99, s98, 8
	v_lshl_add_u32 v149, v234, 4, s99
	v_and_b32_e32 v233, 7, v0
	v_lshl_add_u32 v233, v233, 5, s99
	v_bfe_u32 v235, v0, 3, 1
	v_lshl_add_u32 v151, v235, 4, v233
	s_lshl_b32 s99, s98, 12
	s_add_i32 s99, s99, s76
	v_and_b32_e32 v234, 31, v0
	v_lshl_add_u32 v150, v234, 4, s99
	s_lshr_b32 s99, s38, 5
	s_add_i32 m0, s99, 0x23000
	s_mov_b64 exec, 0xffff
	global_load_lds_dwordx4 v149, s[22:23]
	s_mov_b64 exec, -1
	v_add_u32_e32 v149, 0x100, v149
	s_lshr_b32 s99, s38, 5
	s_add_i32 m0, s99, 0x23100
	s_mov_b64 exec, 0xffff
	global_load_lds_dwordx4 v149, s[22:23]
	s_mov_b64 exec, -1
	v_add_u32_e32 v149, 0x100, v149
	s_lshr_b32 s99, s38, 4
	s_add_i32 m0, s99, 0x21000
	s_mov_b32 exec_hi, 0
	global_load_lds_dwordx4 v150, s[2:3]
	s_mov_b32 exec_hi, -1
	v_add_u32_e32 v150, 0x1000, v150
	s_waitcnt vmcnt(0)
	ds_read_b128 v[66:69], v152
	ds_read_b128 v[70:73], v152 offset:16
	ds_read_b128 v[74:77], v152 offset:256
	ds_read_b128 v[78:81], v152 offset:272
	s_waitcnt lgkmcnt(0)
	s_add_i32 m0, s38, 0x0
	v_mad_u32_u16 v142, v66, v249, v144
	global_load_lds_dwordx4 v142, s[10:11]
	s_add_i32 m0, s38, 0x400
	v_mad_u32_u16 v143, v70, v249, v145
	global_load_lds_dwordx4 v143, s[10:11]
	s_add_i32 m0, s38, 0x800
	v_mad_u32_u16 v142, v66, v249, v144 op_sel:[1,0,0,0]
	global_load_lds_dwordx4 v142, s[10:11]
	s_add_i32 m0, s38, 0xc00
	v_mad_u32_u16 v143, v70, v249, v145 op_sel:[1,0,0,0]
	global_load_lds_dwordx4 v143, s[10:11]
	s_add_i32 m0, s38, 0x1000
	v_mad_u32_u16 v142, v67, v249, v144
	global_load_lds_dwordx4 v142, s[10:11]
	s_add_i32 m0, s38, 0x1400
	v_mad_u32_u16 v143, v71, v249, v145
	global_load_lds_dwordx4 v143, s[10:11]
	s_add_i32 m0, s38, 0x1800
	v_mad_u32_u16 v142, v67, v249, v144 op_sel:[1,0,0,0]
	global_load_lds_dwordx4 v142, s[10:11]
	s_add_i32 m0, s38, 0x1c00
	v_mad_u32_u16 v143, v71, v249, v145 op_sel:[1,0,0,0]
	global_load_lds_dwordx4 v143, s[10:11]
	s_add_i32 m0, s38, 0x2000
	v_mad_u32_u16 v142, v68, v249, v144
	global_load_lds_dwordx4 v142, s[10:11]
	s_add_i32 m0, s38, 0x2400
	v_mad_u32_u16 v143, v72, v249, v145
	global_load_lds_dwordx4 v143, s[10:11]
	s_add_i32 m0, s38, 0x2800
	v_mad_u32_u16 v142, v68, v249, v144 op_sel:[1,0,0,0]
	global_load_lds_dwordx4 v142, s[10:11]
	s_add_i32 m0, s38, 0x2c00
	v_mad_u32_u16 v143, v72, v249, v145 op_sel:[1,0,0,0]
	global_load_lds_dwordx4 v143, s[10:11]
	s_add_i32 m0, s38, 0x3000
	v_mad_u32_u16 v142, v69, v249, v144
	global_load_lds_dwordx4 v142, s[10:11]
	s_add_i32 m0, s38, 0x3400
	v_mad_u32_u16 v143, v73, v249, v145
	global_load_lds_dwordx4 v143, s[10:11]
	s_add_i32 m0, s38, 0x3800
	v_mad_u32_u16 v142, v69, v249, v144 op_sel:[1,0,0,0]
	global_load_lds_dwordx4 v142, s[10:11]
	s_add_i32 m0, s38, 0x3c00
	v_mad_u32_u16 v143, v73, v249, v145 op_sel:[1,0,0,0]
	global_load_lds_dwordx4 v143, s[10:11]
	s_mov_b32 s34, 0
	s_mov_b32 s43, 0
	s_waitcnt vmcnt(0)
	ds_read_b128 v[82:85], v146
	ds_read_b128 v[86:89], v147
	ds_read_b128 v[2:5], v148
	ds_read_b128 v[6:9], v148 offset:16
	ds_read_b128 v[10:13], v148 offset:32
	ds_read_b128 v[14:17], v148 offset:48
	ds_read_b128 v[18:21], v148 offset:256
	ds_read_b128 v[22:25], v148 offset:272
	ds_read_b128 v[26:29], v148 offset:288
	ds_read_b128 v[30:33], v148 offset:304

.Le1_no6:
	s_lshr_b32 s99, s38, 4
	s_add_i32 m0, s99, 0x21200
	s_mov_b32 exec_hi, 0
	global_load_lds_dwordx4 v150, s[2:3]
	s_mov_b32 exec_hi, -1
	v_add_u32_e32 v150, s40, v150
	s_lshr_b32 s99, s38, 5
	s_add_i32 m0, s99, 0x23000
	s_mov_b64 exec, 0xffff
	global_load_lds_dwordx4 v149, s[22:23]
	s_mov_b64 exec, -1
	v_add_u32_e32 v149, 0x100, v149
	s_waitcnt vmcnt(15)
	ds_read_b128 v[90:93], v146 offset:2048
	ds_read_b128 v[94:97], v147 offset:2048
	s_waitcnt lgkmcnt(2)
	s_add_i32 m0, s38, 0x0
	v_mad_u32_u16 v142, v74, v249, v144
	global_load_lds_dwordx4 v142, s[10:11]
	s_add_i32 m0, s38, 0x400
	v_mad_u32_u16 v143, v78, v249, v145
	global_load_lds_dwordx4 v143, s[10:11]
	v_cvt_scalef32_pk_bf16_fp4 v98, v82, 1.0
	v_cvt_scalef32_pk_bf16_fp4 v99, v82, 1.0 op_sel:[1,0,0]
	v_cvt_scalef32_pk_bf16_fp4 v100, v82, 1.0 op_sel:[0,1,0]
	v_cvt_scalef32_pk_bf16_fp4 v101, v82, 1.0 op_sel:[1,1,0]
	v_cvt_scalef32_pk_bf16_fp4 v102, v83, 1.0
	v_cvt_scalef32_pk_bf16_fp4 v103, v83, 1.0 op_sel:[1,0,0]
	v_cvt_scalef32_pk_bf16_fp4 v104, v83, 1.0 op_sel:[0,1,0]
	v_cvt_scalef32_pk_bf16_fp4 v105, v83, 1.0 op_sel:[1,1,0]
	v_mfma_f32_16x16x32_bf16 v[106:109], v[2:5], v[98:101], 0
	v_cvt_scalef32_pk_bf16_fp4 v98, v84, 1.0
	v_cvt_scalef32_pk_bf16_fp4 v99, v84, 1.0 op_sel:[1,0,0]
	v_cvt_scalef32_pk_bf16_fp4 v100, v84, 1.0 op_sel:[0,1,0]
	v_cvt_scalef32_pk_bf16_fp4 v101, v84, 1.0 op_sel:[1,1,0]
	v_mfma_f32_16x16x32_bf16 v[106:109], v[6:9], v[102:105], v[106:109]
	v_cvt_scalef32_pk_bf16_fp4 v102, v85, 1.0
	v_cvt_scalef32_pk_bf16_fp4 v103, v85, 1.0 op_sel:[1,0,0]
	v_cvt_scalef32_pk_bf16_fp4 v104, v85, 1.0 op_sel:[0,1,0]
	v_cvt_scalef32_pk_bf16_fp4 v105, v85, 1.0 op_sel:[1,1,0]
	v_mfma_f32_16x16x32_bf16 v[106:109], v[10:13], v[98:101], v[106:109]
	v_cvt_scalef32_pk_bf16_fp4 v98, v86, 1.0
	v_cvt_scalef32_pk_bf16_fp4 v99, v86, 1.0 op_sel:[1,0,0]
	v_cvt_scalef32_pk_bf16_fp4 v100, v86, 1.0 op_sel:[0,1,0]
	v_cvt_scalef32_pk_bf16_fp4 v101, v86, 1.0 op_sel:[1,1,0]
	v_mfma_f32_16x16x32_bf16 v[106:109], v[14:17], v[102:105], v[106:109]
	v_cvt_scalef32_pk_bf16_fp4 v102, v87, 1.0
	v_cvt_scalef32_pk_bf16_fp4 v103, v87, 1.0 op_sel:[1,0,0]
	v_cvt_scalef32_pk_bf16_fp4 v104, v87, 1.0 op_sel:[0,1,0]
	v_cvt_scalef32_pk_bf16_fp4 v105, v87, 1.0 op_sel:[1,1,0]
	v_mfma_f32_16x16x32_bf16 v[106:109], v[18:21], v[98:101], v[106:109]
	v_cvt_scalef32_pk_bf16_fp4 v98, v88, 1.0
	v_cvt_scalef32_pk_bf16_fp4 v99, v88, 1.0 op_sel:[1,0,0]
	v_cvt_scalef32_pk_bf16_fp4 v100, v88, 1.0 op_sel:[0,1,0]
	v_cvt_scalef32_pk_bf16_fp4 v101, v88, 1.0 op_sel:[1,1,0]
	v_mfma_f32_16x16x32_bf16 v[106:109], v[22:25], v[102:105], v[106:109]
	v_cvt_scalef32_pk_bf16_fp4 v102, v89, 1.0
	v_cvt_scalef32_pk_bf16_fp4 v103, v89, 1.0 op_sel:[1,0,0]
	v_cvt_scalef32_pk_bf16_fp4 v104, v89, 1.0 op_sel:[0,1,0]
	v_cvt_scalef32_pk_bf16_fp4 v105, v89, 1.0 op_sel:[1,1,0]
	v_mfma_f32_16x16x32_bf16 v[106:109], v[26:29], v[98:101], v[106:109]
	v_mfma_f32_16x16x32_bf16 v[106:109], v[30:33], v[102:105], v[106:109]
	s_waitcnt vmcnt(15)
	ds_read_b128 v[82:85], v146 offset:4096
	ds_read_b128 v[86:89], v147 offset:4096
	s_waitcnt lgkmcnt(2)
	s_add_i32 m0, s38, 0x800
	v_mad_u32_u16 v142, v74, v249, v144 op_sel:[1,0,0,0]
	global_load_lds_dwordx4 v142, s[10:11]
	s_add_i32 m0, s38, 0xc00
	v_mad_u32_u16 v143, v78, v249, v145 op_sel:[1,0,0,0]
	global_load_lds_dwordx4 v143, s[10:11]
	v_cvt_scalef32_pk_bf16_fp4 v98, v90, 1.0
	v_cvt_scalef32_pk_bf16_fp4 v99, v90, 1.0 op_sel:[1,0,0]
	v_cvt_scalef32_pk_bf16_fp4 v100, v90, 1.0 op_sel:[0,1,0]
	v_cvt_scalef32_pk_bf16_fp4 v101, v90, 1.0 op_sel:[1,1,0]
	v_cvt_scalef32_pk_bf16_fp4 v102, v91, 1.0
	v_cvt_scalef32_pk_bf16_fp4 v103, v91, 1.0 op_sel:[1,0,0]
	v_cvt_scalef32_pk_bf16_fp4 v104, v91, 1.0 op_sel:[0,1,0]
	v_cvt_scalef32_pk_bf16_fp4 v105, v91, 1.0 op_sel:[1,1,0]
	v_mfma_f32_16x16x32_bf16 v[110:113], v[2:5], v[98:101], 0
	v_cvt_scalef32_pk_bf16_fp4 v98, v92, 1.0
	v_cvt_scalef32_pk_bf16_fp4 v99, v92, 1.0 op_sel:[1,0,0]
	v_cvt_scalef32_pk_bf16_fp4 v100, v92, 1.0 op_sel:[0,1,0]
	v_cvt_scalef32_pk_bf16_fp4 v101, v92, 1.0 op_sel:[1,1,0]
	v_mfma_f32_16x16x32_bf16 v[110:113], v[6:9], v[102:105], v[110:113]
	v_cvt_scalef32_pk_bf16_fp4 v102, v93, 1.0
	v_cvt_scalef32_pk_bf16_fp4 v103, v93, 1.0 op_sel:[1,0,0]
	v_cvt_scalef32_pk_bf16_fp4 v104, v93, 1.0 op_sel:[0,1,0]
	v_cvt_scalef32_pk_bf16_fp4 v105, v93, 1.0 op_sel:[1,1,0]
	v_mfma_f32_16x16x32_bf16 v[110:113], v[10:13], v[98:101], v[110:113]
	v_cvt_scalef32_pk_bf16_fp4 v98, v94, 1.0
	v_cvt_scalef32_pk_bf16_fp4 v99, v94, 1.0 op_sel:[1,0,0]
	v_cvt_scalef32_pk_bf16_fp4 v100, v94, 1.0 op_sel:[0,1,0]
	v_cvt_scalef32_pk_bf16_fp4 v101, v94, 1.0 op_sel:[1,1,0]
	v_mfma_f32_16x16x32_bf16 v[110:113], v[14:17], v[102:105], v[110:113]
	v_cvt_scalef32_pk_bf16_fp4 v102, v95, 1.0
	v_cvt_scalef32_pk_bf16_fp4 v103, v95, 1.0 op_sel:[1,0,0]
	v_cvt_scalef32_pk_bf16_fp4 v104, v95, 1.0 op_sel:[0,1,0]
	v_cvt_scalef32_pk_bf16_fp4 v105, v95, 1.0 op_sel:[1,1,0]
	v_mfma_f32_16x16x32_bf16 v[110:113], v[18:21], v[98:101], v[110:113]
	v_cvt_scalef32_pk_bf16_fp4 v98, v96, 1.0
	v_cvt_scalef32_pk_bf16_fp4 v99, v96, 1.0 op_sel:[1,0,0]
	v_cvt_scalef32_pk_bf16_fp4 v100, v96, 1.0 op_sel:[0,1,0]
	v_cvt_scalef32_pk_bf16_fp4 v101, v96, 1.0 op_sel:[1,1,0]
	v_mfma_f32_16x16x32_bf16 v[110:113], v[22:25], v[102:105], v[110:113]
	v_cvt_scalef32_pk_bf16_fp4 v102, v97, 1.0
	v_cvt_scalef32_pk_bf16_fp4 v103, v97, 1.0 op_sel:[1,0,0]
	v_cvt_scalef32_pk_bf16_fp4 v104, v97, 1.0 op_sel:[0,1,0]
	v_cvt_scalef32_pk_bf16_fp4 v105, v97, 1.0 op_sel:[1,1,0]
	v_mfma_f32_16x16x32_bf16 v[110:113], v[26:29], v[98:101], v[110:113]
	v_mfma_f32_16x16x32_bf16 v[110:113], v[30:33], v[102:105], v[110:113]
	s_waitcnt vmcnt(15)
	ds_read_b128 v[90:93], v146 offset:6144
	ds_read_b128 v[94:97], v147 offset:6144
	s_waitcnt lgkmcnt(2)
	s_add_i32 m0, s38, 0x1000
	v_mad_u32_u16 v142, v75, v249, v144
	global_load_lds_dwordx4 v142, s[10:11]
	s_add_i32 m0, s38, 0x1400
	v_mad_u32_u16 v143, v79, v249, v145
	global_load_lds_dwordx4 v143, s[10:11]
	v_cvt_scalef32_pk_bf16_fp4 v98, v82, 1.0
	v_cvt_scalef32_pk_bf16_fp4 v99, v82, 1.0 op_sel:[1,0,0]
	v_cvt_scalef32_pk_bf16_fp4 v100, v82, 1.0 op_sel:[0,1,0]
	v_cvt_scalef32_pk_bf16_fp4 v101, v82, 1.0 op_sel:[1,1,0]
	v_cvt_scalef32_pk_bf16_fp4 v102, v83, 1.0
	v_cvt_scalef32_pk_bf16_fp4 v103, v83, 1.0 op_sel:[1,0,0]
	v_cvt_scalef32_pk_bf16_fp4 v104, v83, 1.0 op_sel:[0,1,0]
	v_cvt_scalef32_pk_bf16_fp4 v105, v83, 1.0 op_sel:[1,1,0]
	v_mfma_f32_16x16x32_bf16 v[114:117], v[2:5], v[98:101], 0
	v_cvt_scalef32_pk_bf16_fp4 v98, v84, 1.0
	v_cvt_scalef32_pk_bf16_fp4 v99, v84, 1.0 op_sel:[1,0,0]
	v_cvt_scalef32_pk_bf16_fp4 v100, v84, 1.0 op_sel:[0,1,0]
	v_cvt_scalef32_pk_bf16_fp4 v101, v84, 1.0 op_sel:[1,1,0]
	v_mfma_f32_16x16x32_bf16 v[114:117], v[6:9], v[102:105], v[114:117]
	v_cvt_scalef32_pk_bf16_fp4 v102, v85, 1.0
	v_cvt_scalef32_pk_bf16_fp4 v103, v85, 1.0 op_sel:[1,0,0]
	v_cvt_scalef32_pk_bf16_fp4 v104, v85, 1.0 op_sel:[0,1,0]
	v_cvt_scalef32_pk_bf16_fp4 v105, v85, 1.0 op_sel:[1,1,0]
	v_mfma_f32_16x16x32_bf16 v[114:117], v[10:13], v[98:101], v[114:117]
	v_cvt_scalef32_pk_bf16_fp4 v98, v86, 1.0
	v_cvt_scalef32_pk_bf16_fp4 v99, v86, 1.0 op_sel:[1,0,0]
	v_cvt_scalef32_pk_bf16_fp4 v100, v86, 1.0 op_sel:[0,1,0]
	v_cvt_scalef32_pk_bf16_fp4 v101, v86, 1.0 op_sel:[1,1,0]
	v_mfma_f32_16x16x32_bf16 v[114:117], v[14:17], v[102:105], v[114:117]
	v_cvt_scalef32_pk_bf16_fp4 v102, v87, 1.0
	v_cvt_scalef32_pk_bf16_fp4 v103, v87, 1.0 op_sel:[1,0,0]
	v_cvt_scalef32_pk_bf16_fp4 v104, v87, 1.0 op_sel:[0,1,0]
	v_cvt_scalef32_pk_bf16_fp4 v105, v87, 1.0 op_sel:[1,1,0]
	v_mfma_f32_16x16x32_bf16 v[114:117], v[18:21], v[98:101], v[114:117]
	v_cvt_scalef32_pk_bf16_fp4 v98, v88, 1.0
	v_cvt_scalef32_pk_bf16_fp4 v99, v88, 1.0 op_sel:[1,0,0]
	v_cvt_scalef32_pk_bf16_fp4 v100, v88, 1.0 op_sel:[0,1,0]
	v_cvt_scalef32_pk_bf16_fp4 v101, v88, 1.0 op_sel:[1,1,0]
	v_mfma_f32_16x16x32_bf16 v[114:117], v[22:25], v[102:105], v[114:117]
	v_cvt_scalef32_pk_bf16_fp4 v102, v89, 1.0
	v_cvt_scalef32_pk_bf16_fp4 v103, v89, 1.0 op_sel:[1,0,0]
	v_cvt_scalef32_pk_bf16_fp4 v104, v89, 1.0 op_sel:[0,1,0]
	v_cvt_scalef32_pk_bf16_fp4 v105, v89, 1.0 op_sel:[1,1,0]
	v_mfma_f32_16x16x32_bf16 v[114:117], v[26:29], v[98:101], v[114:117]
	v_mfma_f32_16x16x32_bf16 v[114:117], v[30:33], v[102:105], v[114:117]
	s_waitcnt vmcnt(15)
	ds_read_b128 v[82:85], v146 offset:8192
	ds_read_b128 v[86:89], v147 offset:8192
	s_waitcnt lgkmcnt(2)
	s_add_i32 m0, s38, 0x1800
	v_mad_u32_u16 v142, v75, v249, v144 op_sel:[1,0,0,0]
	global_load_lds_dwordx4 v142, s[10:11]
	s_add_i32 m0, s38, 0x1c00
	v_mad_u32_u16 v143, v79, v249, v145 op_sel:[1,0,0,0]
	global_load_lds_dwordx4 v143, s[10:11]
	v_cvt_scalef32_pk_bf16_fp4 v98, v90, 1.0
	v_cvt_scalef32_pk_bf16_fp4 v99, v90, 1.0 op_sel:[1,0,0]
	v_cvt_scalef32_pk_bf16_fp4 v100, v90, 1.0 op_sel:[0,1,0]
	v_cvt_scalef32_pk_bf16_fp4 v101, v90, 1.0 op_sel:[1,1,0]
	v_cvt_scalef32_pk_bf16_fp4 v102, v91, 1.0
	v_cvt_scalef32_pk_bf16_fp4 v103, v91, 1.0 op_sel:[1,0,0]
	v_cvt_scalef32_pk_bf16_fp4 v104, v91, 1.0 op_sel:[0,1,0]
	v_cvt_scalef32_pk_bf16_fp4 v105, v91, 1.0 op_sel:[1,1,0]
	v_mfma_f32_16x16x32_bf16 v[118:121], v[2:5], v[98:101], 0
	v_cvt_scalef32_pk_bf16_fp4 v98, v92, 1.0
	v_cvt_scalef32_pk_bf16_fp4 v99, v92, 1.0 op_sel:[1,0,0]
	v_cvt_scalef32_pk_bf16_fp4 v100, v92, 1.0 op_sel:[0,1,0]
	v_cvt_scalef32_pk_bf16_fp4 v101, v92, 1.0 op_sel:[1,1,0]
	v_mfma_f32_16x16x32_bf16 v[118:121], v[6:9], v[102:105], v[118:121]
	v_cvt_scalef32_pk_bf16_fp4 v102, v93, 1.0
	v_cvt_scalef32_pk_bf16_fp4 v103, v93, 1.0 op_sel:[1,0,0]
	v_cvt_scalef32_pk_bf16_fp4 v104, v93, 1.0 op_sel:[0,1,0]
	v_cvt_scalef32_pk_bf16_fp4 v105, v93, 1.0 op_sel:[1,1,0]
	v_mfma_f32_16x16x32_bf16 v[118:121], v[10:13], v[98:101], v[118:121]
	v_cvt_scalef32_pk_bf16_fp4 v98, v94, 1.0
	v_cvt_scalef32_pk_bf16_fp4 v99, v94, 1.0 op_sel:[1,0,0]
	v_cvt_scalef32_pk_bf16_fp4 v100, v94, 1.0 op_sel:[0,1,0]
	v_cvt_scalef32_pk_bf16_fp4 v101, v94, 1.0 op_sel:[1,1,0]
	v_mfma_f32_16x16x32_bf16 v[118:121], v[14:17], v[102:105], v[118:121]
	v_cvt_scalef32_pk_bf16_fp4 v102, v95, 1.0
	v_cvt_scalef32_pk_bf16_fp4 v103, v95, 1.0 op_sel:[1,0,0]
	v_cvt_scalef32_pk_bf16_fp4 v104, v95, 1.0 op_sel:[0,1,0]
	v_cvt_scalef32_pk_bf16_fp4 v105, v95, 1.0 op_sel:[1,1,0]
	v_mfma_f32_16x16x32_bf16 v[118:121], v[18:21], v[98:101], v[118:121]
	v_cvt_scalef32_pk_bf16_fp4 v98, v96, 1.0
	v_cvt_scalef32_pk_bf16_fp4 v99, v96, 1.0 op_sel:[1,0,0]
	v_cvt_scalef32_pk_bf16_fp4 v100, v96, 1.0 op_sel:[0,1,0]
	v_cvt_scalef32_pk_bf16_fp4 v101, v96, 1.0 op_sel:[1,1,0]
	v_mfma_f32_16x16x32_bf16 v[118:121], v[22:25], v[102:105], v[118:121]
	v_cvt_scalef32_pk_bf16_fp4 v102, v97, 1.0
	v_cvt_scalef32_pk_bf16_fp4 v103, v97, 1.0 op_sel:[1,0,0]
	v_cvt_scalef32_pk_bf16_fp4 v104, v97, 1.0 op_sel:[0,1,0]
	v_cvt_scalef32_pk_bf16_fp4 v105, v97, 1.0 op_sel:[1,1,0]
	v_mfma_f32_16x16x32_bf16 v[118:121], v[26:29], v[98:101], v[118:121]
	v_cvt_pk_bf16_f32 v138, v106, v110
	v_mfma_f32_16x16x32_bf16 v[118:121], v[30:33], v[102:105], v[118:121]
	s_waitcnt vmcnt(15)
	ds_read_b128 v[90:93], v146 offset:10240
	ds_read_b128 v[94:97], v147 offset:10240
	s_waitcnt lgkmcnt(2)
	s_add_i32 m0, s38, 0x2000
	v_mad_u32_u16 v142, v76, v249, v144
	global_load_lds_dwordx4 v142, s[10:11]
	s_add_i32 m0, s38, 0x2400
	v_mad_u32_u16 v143, v80, v249, v145
	global_load_lds_dwordx4 v143, s[10:11]
	v_cvt_scalef32_pk_bf16_fp4 v98, v82, 1.0
	v_cvt_scalef32_pk_bf16_fp4 v99, v82, 1.0 op_sel:[1,0,0]
	v_cvt_scalef32_pk_bf16_fp4 v100, v82, 1.0 op_sel:[0,1,0]
	v_cvt_scalef32_pk_bf16_fp4 v101, v82, 1.0 op_sel:[1,1,0]
	v_cvt_scalef32_pk_bf16_fp4 v102, v83, 1.0
	v_cvt_scalef32_pk_bf16_fp4 v103, v83, 1.0 op_sel:[1,0,0]
	v_cvt_scalef32_pk_bf16_fp4 v104, v83, 1.0 op_sel:[0,1,0]
	v_cvt_scalef32_pk_bf16_fp4 v105, v83, 1.0 op_sel:[1,1,0]
	v_mfma_f32_16x16x32_bf16 v[122:125], v[2:5], v[98:101], 0
	v_cvt_scalef32_pk_bf16_fp4 v98, v84, 1.0
	v_cvt_scalef32_pk_bf16_fp4 v99, v84, 1.0 op_sel:[1,0,0]
	v_cvt_scalef32_pk_bf16_fp4 v100, v84, 1.0 op_sel:[0,1,0]
	v_cvt_scalef32_pk_bf16_fp4 v101, v84, 1.0 op_sel:[1,1,0]
	v_mfma_f32_16x16x32_bf16 v[122:125], v[6:9], v[102:105], v[122:125]
	v_cvt_scalef32_pk_bf16_fp4 v102, v85, 1.0
	v_cvt_scalef32_pk_bf16_fp4 v103, v85, 1.0 op_sel:[1,0,0]
	v_cvt_scalef32_pk_bf16_fp4 v104, v85, 1.0 op_sel:[0,1,0]
	v_cvt_scalef32_pk_bf16_fp4 v105, v85, 1.0 op_sel:[1,1,0]
	v_mfma_f32_16x16x32_bf16 v[122:125], v[10:13], v[98:101], v[122:125]
	v_cvt_scalef32_pk_bf16_fp4 v98, v86, 1.0
	v_cvt_scalef32_pk_bf16_fp4 v99, v86, 1.0 op_sel:[1,0,0]
	v_cvt_scalef32_pk_bf16_fp4 v100, v86, 1.0 op_sel:[0,1,0]
	v_cvt_scalef32_pk_bf16_fp4 v101, v86, 1.0 op_sel:[1,1,0]
	v_mfma_f32_16x16x32_bf16 v[122:125], v[14:17], v[102:105], v[122:125]
	v_cvt_scalef32_pk_bf16_fp4 v102, v87, 1.0
	v_cvt_scalef32_pk_bf16_fp4 v103, v87, 1.0 op_sel:[1,0,0]
	v_cvt_scalef32_pk_bf16_fp4 v104, v87, 1.0 op_sel:[0,1,0]
	v_cvt_scalef32_pk_bf16_fp4 v105, v87, 1.0 op_sel:[1,1,0]
	v_mfma_f32_16x16x32_bf16 v[122:125], v[18:21], v[98:101], v[122:125]
	v_cvt_scalef32_pk_bf16_fp4 v98, v88, 1.0
	v_cvt_scalef32_pk_bf16_fp4 v99, v88, 1.0 op_sel:[1,0,0]
	v_cvt_scalef32_pk_bf16_fp4 v100, v88, 1.0 op_sel:[0,1,0]
	v_cvt_scalef32_pk_bf16_fp4 v101, v88, 1.0 op_sel:[1,1,0]
	v_mfma_f32_16x16x32_bf16 v[122:125], v[22:25], v[102:105], v[122:125]
	v_cvt_scalef32_pk_bf16_fp4 v102, v89, 1.0
	v_cvt_scalef32_pk_bf16_fp4 v103, v89, 1.0 op_sel:[1,0,0]
	v_cvt_scalef32_pk_bf16_fp4 v104, v89, 1.0 op_sel:[0,1,0]
	v_cvt_scalef32_pk_bf16_fp4 v105, v89, 1.0 op_sel:[1,1,0]
	v_mfma_f32_16x16x32_bf16 v[122:125], v[26:29], v[98:101], v[122:125]
	v_mfma_f32_16x16x32_bf16 v[122:125], v[30:33], v[102:105], v[122:125]
	s_waitcnt vmcnt(15)
	ds_read_b128 v[82:85], v146 offset:12288
	ds_read_b128 v[86:89], v147 offset:12288
	s_waitcnt lgkmcnt(2)
	s_add_i32 m0, s38, 0x2800
	v_mad_u32_u16 v142, v76, v249, v144 op_sel:[1,0,0,0]
	global_load_lds_dwordx4 v142, s[10:11]
	s_add_i32 m0, s38, 0x2c00
	v_mad_u32_u16 v143, v80, v249, v145 op_sel:[1,0,0,0]
	global_load_lds_dwordx4 v143, s[10:11]
	v_cvt_scalef32_pk_bf16_fp4 v98, v90, 1.0
	v_cvt_scalef32_pk_bf16_fp4 v99, v90, 1.0 op_sel:[1,0,0]
	v_cvt_scalef32_pk_bf16_fp4 v100, v90, 1.0 op_sel:[0,1,0]
	v_cvt_scalef32_pk_bf16_fp4 v101, v90, 1.0 op_sel:[1,1,0]
	v_cvt_scalef32_pk_bf16_fp4 v102, v91, 1.0
	v_cvt_scalef32_pk_bf16_fp4 v103, v91, 1.0 op_sel:[1,0,0]
	v_cvt_scalef32_pk_bf16_fp4 v104, v91, 1.0 op_sel:[0,1,0]
	v_cvt_scalef32_pk_bf16_fp4 v105, v91, 1.0 op_sel:[1,1,0]
	v_mfma_f32_16x16x32_bf16 v[126:129], v[2:5], v[98:101], 0
	v_cvt_scalef32_pk_bf16_fp4 v98, v92, 1.0
	v_cvt_scalef32_pk_bf16_fp4 v99, v92, 1.0 op_sel:[1,0,0]
	v_cvt_scalef32_pk_bf16_fp4 v100, v92, 1.0 op_sel:[0,1,0]
	v_cvt_scalef32_pk_bf16_fp4 v101, v92, 1.0 op_sel:[1,1,0]
	v_mfma_f32_16x16x32_bf16 v[126:129], v[6:9], v[102:105], v[126:129]
	v_cvt_scalef32_pk_bf16_fp4 v102, v93, 1.0
	v_cvt_scalef32_pk_bf16_fp4 v103, v93, 1.0 op_sel:[1,0,0]
	v_cvt_scalef32_pk_bf16_fp4 v104, v93, 1.0 op_sel:[0,1,0]
	v_cvt_scalef32_pk_bf16_fp4 v105, v93, 1.0 op_sel:[1,1,0]
	v_mfma_f32_16x16x32_bf16 v[126:129], v[10:13], v[98:101], v[126:129]
	v_cvt_scalef32_pk_bf16_fp4 v98, v94, 1.0
	v_cvt_scalef32_pk_bf16_fp4 v99, v94, 1.0 op_sel:[1,0,0]
	v_cvt_scalef32_pk_bf16_fp4 v100, v94, 1.0 op_sel:[0,1,0]
	v_cvt_scalef32_pk_bf16_fp4 v101, v94, 1.0 op_sel:[1,1,0]
	v_mfma_f32_16x16x32_bf16 v[126:129], v[14:17], v[102:105], v[126:129]
	v_cvt_scalef32_pk_bf16_fp4 v102, v95, 1.0
	v_cvt_scalef32_pk_bf16_fp4 v103, v95, 1.0 op_sel:[1,0,0]
	v_cvt_scalef32_pk_bf16_fp4 v104, v95, 1.0 op_sel:[0,1,0]
	v_cvt_scalef32_pk_bf16_fp4 v105, v95, 1.0 op_sel:[1,1,0]
	v_mfma_f32_16x16x32_bf16 v[126:129], v[18:21], v[98:101], v[126:129]
	v_cvt_scalef32_pk_bf16_fp4 v98, v96, 1.0
	v_cvt_scalef32_pk_bf16_fp4 v99, v96, 1.0 op_sel:[1,0,0]
	v_cvt_scalef32_pk_bf16_fp4 v100, v96, 1.0 op_sel:[0,1,0]
	v_cvt_scalef32_pk_bf16_fp4 v101, v96, 1.0 op_sel:[1,1,0]
	v_mfma_f32_16x16x32_bf16 v[126:129], v[22:25], v[102:105], v[126:129]
	v_cvt_scalef32_pk_bf16_fp4 v102, v97, 1.0
	v_cvt_scalef32_pk_bf16_fp4 v103, v97, 1.0 op_sel:[1,0,0]
	v_cvt_scalef32_pk_bf16_fp4 v104, v97, 1.0 op_sel:[0,1,0]
	v_cvt_scalef32_pk_bf16_fp4 v105, v97, 1.0 op_sel:[1,1,0]
	v_mfma_f32_16x16x32_bf16 v[126:129], v[26:29], v[98:101], v[126:129]
	v_cvt_pk_bf16_f32 v139, v114, v118
	v_mfma_f32_16x16x32_bf16 v[126:129], v[30:33], v[102:105], v[126:129]
	s_waitcnt vmcnt(15)
	ds_read_b128 v[90:93], v146 offset:14336
	ds_read_b128 v[94:97], v147 offset:14336
	s_waitcnt lgkmcnt(2)
	s_add_i32 m0, s38, 0x3000
	v_mad_u32_u16 v142, v77, v249, v144
	global_load_lds_dwordx4 v142, s[10:11]
	s_add_i32 m0, s38, 0x3400
	v_mad_u32_u16 v143, v81, v249, v145
	global_load_lds_dwordx4 v143, s[10:11]
	v_cvt_scalef32_pk_bf16_fp4 v98, v82, 1.0
	v_cvt_scalef32_pk_bf16_fp4 v99, v82, 1.0 op_sel:[1,0,0]
	v_cvt_scalef32_pk_bf16_fp4 v100, v82, 1.0 op_sel:[0,1,0]
	v_cvt_scalef32_pk_bf16_fp4 v101, v82, 1.0 op_sel:[1,1,0]
	v_cvt_scalef32_pk_bf16_fp4 v102, v83, 1.0
	v_cvt_scalef32_pk_bf16_fp4 v103, v83, 1.0 op_sel:[1,0,0]
	v_cvt_scalef32_pk_bf16_fp4 v104, v83, 1.0 op_sel:[0,1,0]
	v_cvt_scalef32_pk_bf16_fp4 v105, v83, 1.0 op_sel:[1,1,0]
	v_mfma_f32_16x16x32_bf16 v[130:133], v[2:5], v[98:101], 0
	v_cvt_scalef32_pk_bf16_fp4 v98, v84, 1.0
	v_cvt_scalef32_pk_bf16_fp4 v99, v84, 1.0 op_sel:[1,0,0]
	v_cvt_scalef32_pk_bf16_fp4 v100, v84, 1.0 op_sel:[0,1,0]
	v_cvt_scalef32_pk_bf16_fp4 v101, v84, 1.0 op_sel:[1,1,0]
	v_mfma_f32_16x16x32_bf16 v[130:133], v[6:9], v[102:105], v[130:133]
	v_cvt_scalef32_pk_bf16_fp4 v102, v85, 1.0
	v_cvt_scalef32_pk_bf16_fp4 v103, v85, 1.0 op_sel:[1,0,0]
	v_cvt_scalef32_pk_bf16_fp4 v104, v85, 1.0 op_sel:[0,1,0]
	v_cvt_scalef32_pk_bf16_fp4 v105, v85, 1.0 op_sel:[1,1,0]
	v_mfma_f32_16x16x32_bf16 v[130:133], v[10:13], v[98:101], v[130:133]
	v_cvt_scalef32_pk_bf16_fp4 v98, v86, 1.0
	v_cvt_scalef32_pk_bf16_fp4 v99, v86, 1.0 op_sel:[1,0,0]
	v_cvt_scalef32_pk_bf16_fp4 v100, v86, 1.0 op_sel:[0,1,0]
	v_cvt_scalef32_pk_bf16_fp4 v101, v86, 1.0 op_sel:[1,1,0]
	v_mfma_f32_16x16x32_bf16 v[130:133], v[14:17], v[102:105], v[130:133]
	v_cvt_scalef32_pk_bf16_fp4 v102, v87, 1.0
	v_cvt_scalef32_pk_bf16_fp4 v103, v87, 1.0 op_sel:[1,0,0]
	v_cvt_scalef32_pk_bf16_fp4 v104, v87, 1.0 op_sel:[0,1,0]
	v_cvt_scalef32_pk_bf16_fp4 v105, v87, 1.0 op_sel:[1,1,0]
	v_mfma_f32_16x16x32_bf16 v[130:133], v[18:21], v[98:101], v[130:133]
	v_cvt_scalef32_pk_bf16_fp4 v98, v88, 1.0
	v_cvt_scalef32_pk_bf16_fp4 v99, v88, 1.0 op_sel:[1,0,0]
	v_cvt_scalef32_pk_bf16_fp4 v100, v88, 1.0 op_sel:[0,1,0]
	v_cvt_scalef32_pk_bf16_fp4 v101, v88, 1.0 op_sel:[1,1,0]
	v_mfma_f32_16x16x32_bf16 v[130:133], v[22:25], v[102:105], v[130:133]
	v_cvt_scalef32_pk_bf16_fp4 v102, v89, 1.0
	v_cvt_scalef32_pk_bf16_fp4 v103, v89, 1.0 op_sel:[1,0,0]
	v_cvt_scalef32_pk_bf16_fp4 v104, v89, 1.0 op_sel:[0,1,0]
	v_cvt_scalef32_pk_bf16_fp4 v105, v89, 1.0 op_sel:[1,1,0]
	v_mfma_f32_16x16x32_bf16 v[130:133], v[26:29], v[98:101], v[130:133]
	v_mfma_f32_16x16x32_bf16 v[130:133], v[30:33], v[102:105], v[130:133]
	s_waitcnt vmcnt(12)
	ds_read_b128 v[82:85], v146
	ds_read_b128 v[86:89], v147
	s_waitcnt lgkmcnt(2)
	s_add_i32 m0, s38, 0x3800
	v_mad_u32_u16 v142, v77, v249, v144 op_sel:[1,0,0,0]
	global_load_lds_dwordx4 v142, s[10:11]
	s_add_i32 m0, s38, 0x3c00
	v_mad_u32_u16 v143, v81, v249, v145 op_sel:[1,0,0,0]
	global_load_lds_dwordx4 v143, s[10:11]
	ds_read_b128 v[34:37], v148 offset:512
	ds_read_b128 v[38:41], v148 offset:528
	ds_read_b128 v[42:45], v148 offset:544
	ds_read_b128 v[46:49], v148 offset:560
	ds_read_b128 v[50:53], v148 offset:768
	ds_read_b128 v[54:57], v148 offset:784
	ds_read_b128 v[58:61], v148 offset:800
	ds_read_b128 v[62:65], v148 offset:816
	ds_read_b128 v[66:69], v152
	ds_read_b128 v[70:73], v152 offset:16
	v_cvt_scalef32_pk_bf16_fp4 v98, v90, 1.0
	v_cvt_scalef32_pk_bf16_fp4 v99, v90, 1.0 op_sel:[1,0,0]
	v_cvt_scalef32_pk_bf16_fp4 v100, v90, 1.0 op_sel:[0,1,0]
	v_cvt_scalef32_pk_bf16_fp4 v101, v90, 1.0 op_sel:[1,1,0]
	v_cvt_scalef32_pk_bf16_fp4 v102, v91, 1.0
	v_cvt_scalef32_pk_bf16_fp4 v103, v91, 1.0 op_sel:[1,0,0]
	v_cvt_scalef32_pk_bf16_fp4 v104, v91, 1.0 op_sel:[0,1,0]
	v_cvt_scalef32_pk_bf16_fp4 v105, v91, 1.0 op_sel:[1,1,0]
	v_mfma_f32_16x16x32_bf16 v[134:137], v[2:5], v[98:101], 0
	v_cvt_scalef32_pk_bf16_fp4 v98, v92, 1.0
	v_cvt_scalef32_pk_bf16_fp4 v99, v92, 1.0 op_sel:[1,0,0]
	v_cvt_scalef32_pk_bf16_fp4 v100, v92, 1.0 op_sel:[0,1,0]
	v_cvt_scalef32_pk_bf16_fp4 v101, v92, 1.0 op_sel:[1,1,0]
	v_mfma_f32_16x16x32_bf16 v[134:137], v[6:9], v[102:105], v[134:137]
	v_cvt_scalef32_pk_bf16_fp4 v102, v93, 1.0
	v_cvt_scalef32_pk_bf16_fp4 v103, v93, 1.0 op_sel:[1,0,0]
	v_cvt_scalef32_pk_bf16_fp4 v104, v93, 1.0 op_sel:[0,1,0]
	v_cvt_scalef32_pk_bf16_fp4 v105, v93, 1.0 op_sel:[1,1,0]
	v_mfma_f32_16x16x32_bf16 v[134:137], v[10:13], v[98:101], v[134:137]
	v_cvt_scalef32_pk_bf16_fp4 v98, v94, 1.0
	v_cvt_scalef32_pk_bf16_fp4 v99, v94, 1.0 op_sel:[1,0,0]
	v_cvt_scalef32_pk_bf16_fp4 v100, v94, 1.0 op_sel:[0,1,0]
	v_cvt_scalef32_pk_bf16_fp4 v101, v94, 1.0 op_sel:[1,1,0]
	v_mfma_f32_16x16x32_bf16 v[134:137], v[14:17], v[102:105], v[134:137]
	v_cvt_scalef32_pk_bf16_fp4 v102, v95, 1.0
	v_cvt_scalef32_pk_bf16_fp4 v103, v95, 1.0 op_sel:[1,0,0]
	v_cvt_scalef32_pk_bf16_fp4 v104, v95, 1.0 op_sel:[0,1,0]
	v_cvt_scalef32_pk_bf16_fp4 v105, v95, 1.0 op_sel:[1,1,0]
	v_mfma_f32_16x16x32_bf16 v[134:137], v[18:21], v[98:101], v[134:137]
	v_cvt_scalef32_pk_bf16_fp4 v98, v96, 1.0
	v_cvt_scalef32_pk_bf16_fp4 v99, v96, 1.0 op_sel:[1,0,0]
	v_cvt_scalef32_pk_bf16_fp4 v100, v96, 1.0 op_sel:[0,1,0]
	v_cvt_scalef32_pk_bf16_fp4 v101, v96, 1.0 op_sel:[1,1,0]
	v_mfma_f32_16x16x32_bf16 v[134:137], v[22:25], v[102:105], v[134:137]
	v_cvt_scalef32_pk_bf16_fp4 v102, v97, 1.0
	v_cvt_scalef32_pk_bf16_fp4 v103, v97, 1.0 op_sel:[1,0,0]
	v_cvt_scalef32_pk_bf16_fp4 v104, v97, 1.0 op_sel:[0,1,0]
	v_cvt_scalef32_pk_bf16_fp4 v105, v97, 1.0 op_sel:[1,1,0]
	v_mfma_f32_16x16x32_bf16 v[134:137], v[26:29], v[98:101], v[134:137]
	v_cvt_pk_bf16_f32 v140, v122, v126
	v_mfma_f32_16x16x32_bf16 v[134:137], v[30:33], v[102:105], v[134:137]
	s_nop 7
	s_nop 7
	v_cvt_pk_bf16_f32 v141, v130, v134
	s_mov_b64 exec, 0xffff
	global_store_dwordx4 v151, v[138:141], s[4:5]
	s_mov_b64 exec, -1
	v_add_u32_e32 v151, 0x100, v151
	s_lshr_b32 s99, s38, 4
	s_add_i32 m0, s99, 0x21000
	s_mov_b32 exec_hi, 0
	global_load_lds_dwordx4 v150, s[2:3]
	s_mov_b32 exec_hi, -1
	v_add_u32_e32 v150, 0x1000, v150
	s_lshr_b32 s99, s38, 5
	s_add_i32 m0, s99, 0x23100
	s_mov_b64 exec, 0xffff
	global_load_lds_dwordx4 v149, s[22:23]
	s_mov_b64 exec, -1
	v_add_u32_e32 v149, s41, v149
	s_waitcnt vmcnt(15)
	ds_read_b128 v[90:93], v146 offset:2048
	ds_read_b128 v[94:97], v147 offset:2048
	s_waitcnt lgkmcnt(2)
	s_add_i32 m0, s38, 0x0
	v_mad_u32_u16 v142, v66, v249, v144
	global_load_lds_dwordx4 v142, s[10:11]
	s_add_i32 m0, s38, 0x400
	v_mad_u32_u16 v143, v70, v249, v145
	global_load_lds_dwordx4 v143, s[10:11]
	v_cvt_scalef32_pk_bf16_fp4 v98, v82, 1.0
	v_cvt_scalef32_pk_bf16_fp4 v99, v82, 1.0 op_sel:[1,0,0]
	v_cvt_scalef32_pk_bf16_fp4 v100, v82, 1.0 op_sel:[0,1,0]
	v_cvt_scalef32_pk_bf16_fp4 v101, v82, 1.0 op_sel:[1,1,0]
	v_cvt_scalef32_pk_bf16_fp4 v102, v83, 1.0
	v_cvt_scalef32_pk_bf16_fp4 v103, v83, 1.0 op_sel:[1,0,0]
	v_cvt_scalef32_pk_bf16_fp4 v104, v83, 1.0 op_sel:[0,1,0]
	v_cvt_scalef32_pk_bf16_fp4 v105, v83, 1.0 op_sel:[1,1,0]
	v_mfma_f32_16x16x32_bf16 v[106:109], v[34:37], v[98:101], 0
	v_cvt_scalef32_pk_bf16_fp4 v98, v84, 1.0
	v_cvt_scalef32_pk_bf16_fp4 v99, v84, 1.0 op_sel:[1,0,0]
	v_cvt_scalef32_pk_bf16_fp4 v100, v84, 1.0 op_sel:[0,1,0]
	v_cvt_scalef32_pk_bf16_fp4 v101, v84, 1.0 op_sel:[1,1,0]
	v_mfma_f32_16x16x32_bf16 v[106:109], v[38:41], v[102:105], v[106:109]
	v_cvt_scalef32_pk_bf16_fp4 v102, v85, 1.0
	v_cvt_scalef32_pk_bf16_fp4 v103, v85, 1.0 op_sel:[1,0,0]
	v_cvt_scalef32_pk_bf16_fp4 v104, v85, 1.0 op_sel:[0,1,0]
	v_cvt_scalef32_pk_bf16_fp4 v105, v85, 1.0 op_sel:[1,1,0]
	v_mfma_f32_16x16x32_bf16 v[106:109], v[42:45], v[98:101], v[106:109]
	v_cvt_scalef32_pk_bf16_fp4 v98, v86, 1.0
	v_cvt_scalef32_pk_bf16_fp4 v99, v86, 1.0 op_sel:[1,0,0]
	v_cvt_scalef32_pk_bf16_fp4 v100, v86, 1.0 op_sel:[0,1,0]
	v_cvt_scalef32_pk_bf16_fp4 v101, v86, 1.0 op_sel:[1,1,0]
	v_mfma_f32_16x16x32_bf16 v[106:109], v[46:49], v[102:105], v[106:109]
	v_cvt_scalef32_pk_bf16_fp4 v102, v87, 1.0
	v_cvt_scalef32_pk_bf16_fp4 v103, v87, 1.0 op_sel:[1,0,0]
	v_cvt_scalef32_pk_bf16_fp4 v104, v87, 1.0 op_sel:[0,1,0]
	v_cvt_scalef32_pk_bf16_fp4 v105, v87, 1.0 op_sel:[1,1,0]
	v_mfma_f32_16x16x32_bf16 v[106:109], v[50:53], v[98:101], v[106:109]
	v_cvt_scalef32_pk_bf16_fp4 v98, v88, 1.0
	v_cvt_scalef32_pk_bf16_fp4 v99, v88, 1.0 op_sel:[1,0,0]
	v_cvt_scalef32_pk_bf16_fp4 v100, v88, 1.0 op_sel:[0,1,0]
	v_cvt_scalef32_pk_bf16_fp4 v101, v88, 1.0 op_sel:[1,1,0]
	v_mfma_f32_16x16x32_bf16 v[106:109], v[54:57], v[102:105], v[106:109]
	v_cvt_scalef32_pk_bf16_fp4 v102, v89, 1.0
	v_cvt_scalef32_pk_bf16_fp4 v103, v89, 1.0 op_sel:[1,0,0]
	v_cvt_scalef32_pk_bf16_fp4 v104, v89, 1.0 op_sel:[0,1,0]
	v_cvt_scalef32_pk_bf16_fp4 v105, v89, 1.0 op_sel:[1,1,0]
	v_mfma_f32_16x16x32_bf16 v[106:109], v[58:61], v[98:101], v[106:109]
	v_mfma_f32_16x16x32_bf16 v[106:109], v[62:65], v[102:105], v[106:109]
	s_waitcnt vmcnt(15)
	ds_read_b128 v[82:85], v146 offset:4096
	ds_read_b128 v[86:89], v147 offset:4096
	s_waitcnt lgkmcnt(2)
	s_add_i32 m0, s38, 0x800
	v_mad_u32_u16 v142, v66, v249, v144 op_sel:[1,0,0,0]
	global_load_lds_dwordx4 v142, s[10:11]
	s_add_i32 m0, s38, 0xc00
	v_mad_u32_u16 v143, v70, v249, v145 op_sel:[1,0,0,0]
	global_load_lds_dwordx4 v143, s[10:11]
	v_cvt_scalef32_pk_bf16_fp4 v98, v90, 1.0
	v_cvt_scalef32_pk_bf16_fp4 v99, v90, 1.0 op_sel:[1,0,0]
	v_cvt_scalef32_pk_bf16_fp4 v100, v90, 1.0 op_sel:[0,1,0]
	v_cvt_scalef32_pk_bf16_fp4 v101, v90, 1.0 op_sel:[1,1,0]
	v_cvt_scalef32_pk_bf16_fp4 v102, v91, 1.0
	v_cvt_scalef32_pk_bf16_fp4 v103, v91, 1.0 op_sel:[1,0,0]
	v_cvt_scalef32_pk_bf16_fp4 v104, v91, 1.0 op_sel:[0,1,0]
	v_cvt_scalef32_pk_bf16_fp4 v105, v91, 1.0 op_sel:[1,1,0]
	v_mfma_f32_16x16x32_bf16 v[110:113], v[34:37], v[98:101], 0
	v_cvt_scalef32_pk_bf16_fp4 v98, v92, 1.0
	v_cvt_scalef32_pk_bf16_fp4 v99, v92, 1.0 op_sel:[1,0,0]
	v_cvt_scalef32_pk_bf16_fp4 v100, v92, 1.0 op_sel:[0,1,0]
	v_cvt_scalef32_pk_bf16_fp4 v101, v92, 1.0 op_sel:[1,1,0]
	v_mfma_f32_16x16x32_bf16 v[110:113], v[38:41], v[102:105], v[110:113]
	v_cvt_scalef32_pk_bf16_fp4 v102, v93, 1.0
	v_cvt_scalef32_pk_bf16_fp4 v103, v93, 1.0 op_sel:[1,0,0]
	v_cvt_scalef32_pk_bf16_fp4 v104, v93, 1.0 op_sel:[0,1,0]
	v_cvt_scalef32_pk_bf16_fp4 v105, v93, 1.0 op_sel:[1,1,0]
	v_mfma_f32_16x16x32_bf16 v[110:113], v[42:45], v[98:101], v[110:113]
	v_cvt_scalef32_pk_bf16_fp4 v98, v94, 1.0
	v_cvt_scalef32_pk_bf16_fp4 v99, v94, 1.0 op_sel:[1,0,0]
	v_cvt_scalef32_pk_bf16_fp4 v100, v94, 1.0 op_sel:[0,1,0]
	v_cvt_scalef32_pk_bf16_fp4 v101, v94, 1.0 op_sel:[1,1,0]
	v_mfma_f32_16x16x32_bf16 v[110:113], v[46:49], v[102:105], v[110:113]
	v_cvt_scalef32_pk_bf16_fp4 v102, v95, 1.0
	v_cvt_scalef32_pk_bf16_fp4 v103, v95, 1.0 op_sel:[1,0,0]
	v_cvt_scalef32_pk_bf16_fp4 v104, v95, 1.0 op_sel:[0,1,0]
	v_cvt_scalef32_pk_bf16_fp4 v105, v95, 1.0 op_sel:[1,1,0]
	v_mfma_f32_16x16x32_bf16 v[110:113], v[50:53], v[98:101], v[110:113]
	v_cvt_scalef32_pk_bf16_fp4 v98, v96, 1.0
	v_cvt_scalef32_pk_bf16_fp4 v99, v96, 1.0 op_sel:[1,0,0]
	v_cvt_scalef32_pk_bf16_fp4 v100, v96, 1.0 op_sel:[0,1,0]
	v_cvt_scalef32_pk_bf16_fp4 v101, v96, 1.0 op_sel:[1,1,0]
	v_mfma_f32_16x16x32_bf16 v[110:113], v[54:57], v[102:105], v[110:113]
	v_cvt_scalef32_pk_bf16_fp4 v102, v97, 1.0
	v_cvt_scalef32_pk_bf16_fp4 v103, v97, 1.0 op_sel:[1,0,0]
	v_cvt_scalef32_pk_bf16_fp4 v104, v97, 1.0 op_sel:[0,1,0]
	v_cvt_scalef32_pk_bf16_fp4 v105, v97, 1.0 op_sel:[1,1,0]
	v_mfma_f32_16x16x32_bf16 v[110:113], v[58:61], v[98:101], v[110:113]
	v_mfma_f32_16x16x32_bf16 v[110:113], v[62:65], v[102:105], v[110:113]
	s_waitcnt vmcnt(15)
	ds_read_b128 v[90:93], v146 offset:6144
	ds_read_b128 v[94:97], v147 offset:6144
	s_waitcnt lgkmcnt(2)
	s_add_i32 m0, s38, 0x1000
	v_mad_u32_u16 v142, v67, v249, v144
	global_load_lds_dwordx4 v142, s[10:11]
	s_add_i32 m0, s38, 0x1400
	v_mad_u32_u16 v143, v71, v249, v145
	global_load_lds_dwordx4 v143, s[10:11]
	v_cvt_scalef32_pk_bf16_fp4 v98, v82, 1.0
	v_cvt_scalef32_pk_bf16_fp4 v99, v82, 1.0 op_sel:[1,0,0]
	v_cvt_scalef32_pk_bf16_fp4 v100, v82, 1.0 op_sel:[0,1,0]
	v_cvt_scalef32_pk_bf16_fp4 v101, v82, 1.0 op_sel:[1,1,0]
	v_cvt_scalef32_pk_bf16_fp4 v102, v83, 1.0
	v_cvt_scalef32_pk_bf16_fp4 v103, v83, 1.0 op_sel:[1,0,0]
	v_cvt_scalef32_pk_bf16_fp4 v104, v83, 1.0 op_sel:[0,1,0]
	v_cvt_scalef32_pk_bf16_fp4 v105, v83, 1.0 op_sel:[1,1,0]
	v_mfma_f32_16x16x32_bf16 v[114:117], v[34:37], v[98:101], 0
	v_cvt_scalef32_pk_bf16_fp4 v98, v84, 1.0
	v_cvt_scalef32_pk_bf16_fp4 v99, v84, 1.0 op_sel:[1,0,0]
	v_cvt_scalef32_pk_bf16_fp4 v100, v84, 1.0 op_sel:[0,1,0]
	v_cvt_scalef32_pk_bf16_fp4 v101, v84, 1.0 op_sel:[1,1,0]
	v_mfma_f32_16x16x32_bf16 v[114:117], v[38:41], v[102:105], v[114:117]
	v_cvt_scalef32_pk_bf16_fp4 v102, v85, 1.0
	v_cvt_scalef32_pk_bf16_fp4 v103, v85, 1.0 op_sel:[1,0,0]
	v_cvt_scalef32_pk_bf16_fp4 v104, v85, 1.0 op_sel:[0,1,0]
	v_cvt_scalef32_pk_bf16_fp4 v105, v85, 1.0 op_sel:[1,1,0]
	v_mfma_f32_16x16x32_bf16 v[114:117], v[42:45], v[98:101], v[114:117]
	v_cvt_scalef32_pk_bf16_fp4 v98, v86, 1.0
	v_cvt_scalef32_pk_bf16_fp4 v99, v86, 1.0 op_sel:[1,0,0]
	v_cvt_scalef32_pk_bf16_fp4 v100, v86, 1.0 op_sel:[0,1,0]
	v_cvt_scalef32_pk_bf16_fp4 v101, v86, 1.0 op_sel:[1,1,0]
	v_mfma_f32_16x16x32_bf16 v[114:117], v[46:49], v[102:105], v[114:117]
	v_cvt_scalef32_pk_bf16_fp4 v102, v87, 1.0
	v_cvt_scalef32_pk_bf16_fp4 v103, v87, 1.0 op_sel:[1,0,0]
	v_cvt_scalef32_pk_bf16_fp4 v104, v87, 1.0 op_sel:[0,1,0]
	v_cvt_scalef32_pk_bf16_fp4 v105, v87, 1.0 op_sel:[1,1,0]
	v_mfma_f32_16x16x32_bf16 v[114:117], v[50:53], v[98:101], v[114:117]
	v_cvt_scalef32_pk_bf16_fp4 v98, v88, 1.0
	v_cvt_scalef32_pk_bf16_fp4 v99, v88, 1.0 op_sel:[1,0,0]
	v_cvt_scalef32_pk_bf16_fp4 v100, v88, 1.0 op_sel:[0,1,0]
	v_cvt_scalef32_pk_bf16_fp4 v101, v88, 1.0 op_sel:[1,1,0]
	v_mfma_f32_16x16x32_bf16 v[114:117], v[54:57], v[102:105], v[114:117]
	v_cvt_scalef32_pk_bf16_fp4 v102, v89, 1.0
	v_cvt_scalef32_pk_bf16_fp4 v103, v89, 1.0 op_sel:[1,0,0]
	v_cvt_scalef32_pk_bf16_fp4 v104, v89, 1.0 op_sel:[0,1,0]
	v_cvt_scalef32_pk_bf16_fp4 v105, v89, 1.0 op_sel:[1,1,0]
	v_mfma_f32_16x16x32_bf16 v[114:117], v[58:61], v[98:101], v[114:117]
	v_mfma_f32_16x16x32_bf16 v[114:117], v[62:65], v[102:105], v[114:117]
	s_waitcnt vmcnt(15)
	ds_read_b128 v[82:85], v146 offset:8192
	ds_read_b128 v[86:89], v147 offset:8192
	s_waitcnt lgkmcnt(2)
	s_add_i32 m0, s38, 0x1800
	v_mad_u32_u16 v142, v67, v249, v144 op_sel:[1,0,0,0]
	global_load_lds_dwordx4 v142, s[10:11]
	s_add_i32 m0, s38, 0x1c00
	v_mad_u32_u16 v143, v71, v249, v145 op_sel:[1,0,0,0]
	global_load_lds_dwordx4 v143, s[10:11]
	v_cvt_scalef32_pk_bf16_fp4 v98, v90, 1.0
	v_cvt_scalef32_pk_bf16_fp4 v99, v90, 1.0 op_sel:[1,0,0]
	v_cvt_scalef32_pk_bf16_fp4 v100, v90, 1.0 op_sel:[0,1,0]
	v_cvt_scalef32_pk_bf16_fp4 v101, v90, 1.0 op_sel:[1,1,0]
	v_cvt_scalef32_pk_bf16_fp4 v102, v91, 1.0
	v_cvt_scalef32_pk_bf16_fp4 v103, v91, 1.0 op_sel:[1,0,0]
	v_cvt_scalef32_pk_bf16_fp4 v104, v91, 1.0 op_sel:[0,1,0]
	v_cvt_scalef32_pk_bf16_fp4 v105, v91, 1.0 op_sel:[1,1,0]
	v_mfma_f32_16x16x32_bf16 v[118:121], v[34:37], v[98:101], 0
	v_cvt_scalef32_pk_bf16_fp4 v98, v92, 1.0
	v_cvt_scalef32_pk_bf16_fp4 v99, v92, 1.0 op_sel:[1,0,0]
	v_cvt_scalef32_pk_bf16_fp4 v100, v92, 1.0 op_sel:[0,1,0]
	v_cvt_scalef32_pk_bf16_fp4 v101, v92, 1.0 op_sel:[1,1,0]
	v_mfma_f32_16x16x32_bf16 v[118:121], v[38:41], v[102:105], v[118:121]
	v_cvt_scalef32_pk_bf16_fp4 v102, v93, 1.0
	v_cvt_scalef32_pk_bf16_fp4 v103, v93, 1.0 op_sel:[1,0,0]
	v_cvt_scalef32_pk_bf16_fp4 v104, v93, 1.0 op_sel:[0,1,0]
	v_cvt_scalef32_pk_bf16_fp4 v105, v93, 1.0 op_sel:[1,1,0]
	v_mfma_f32_16x16x32_bf16 v[118:121], v[42:45], v[98:101], v[118:121]
	v_cvt_scalef32_pk_bf16_fp4 v98, v94, 1.0
	v_cvt_scalef32_pk_bf16_fp4 v99, v94, 1.0 op_sel:[1,0,0]
	v_cvt_scalef32_pk_bf16_fp4 v100, v94, 1.0 op_sel:[0,1,0]
	v_cvt_scalef32_pk_bf16_fp4 v101, v94, 1.0 op_sel:[1,1,0]
	v_mfma_f32_16x16x32_bf16 v[118:121], v[46:49], v[102:105], v[118:121]
	v_cvt_scalef32_pk_bf16_fp4 v102, v95, 1.0
	v_cvt_scalef32_pk_bf16_fp4 v103, v95, 1.0 op_sel:[1,0,0]
	v_cvt_scalef32_pk_bf16_fp4 v104, v95, 1.0 op_sel:[0,1,0]
	v_cvt_scalef32_pk_bf16_fp4 v105, v95, 1.0 op_sel:[1,1,0]
	v_mfma_f32_16x16x32_bf16 v[118:121], v[50:53], v[98:101], v[118:121]
	v_cvt_scalef32_pk_bf16_fp4 v98, v96, 1.0
	v_cvt_scalef32_pk_bf16_fp4 v99, v96, 1.0 op_sel:[1,0,0]
	v_cvt_scalef32_pk_bf16_fp4 v100, v96, 1.0 op_sel:[0,1,0]
	v_cvt_scalef32_pk_bf16_fp4 v101, v96, 1.0 op_sel:[1,1,0]
	v_mfma_f32_16x16x32_bf16 v[118:121], v[54:57], v[102:105], v[118:121]
	v_cvt_scalef32_pk_bf16_fp4 v102, v97, 1.0
	v_cvt_scalef32_pk_bf16_fp4 v103, v97, 1.0 op_sel:[1,0,0]
	v_cvt_scalef32_pk_bf16_fp4 v104, v97, 1.0 op_sel:[0,1,0]
	v_cvt_scalef32_pk_bf16_fp4 v105, v97, 1.0 op_sel:[1,1,0]
	v_mfma_f32_16x16x32_bf16 v[118:121], v[58:61], v[98:101], v[118:121]
	v_cvt_pk_bf16_f32 v138, v106, v110
	v_mfma_f32_16x16x32_bf16 v[118:121], v[62:65], v[102:105], v[118:121]
	s_waitcnt vmcnt(15)
	ds_read_b128 v[90:93], v146 offset:10240
	ds_read_b128 v[94:97], v147 offset:10240
	s_waitcnt lgkmcnt(2)
	s_add_i32 m0, s38, 0x2000
	v_mad_u32_u16 v142, v68, v249, v144
	global_load_lds_dwordx4 v142, s[10:11]
	s_add_i32 m0, s38, 0x2400
	v_mad_u32_u16 v143, v72, v249, v145
	global_load_lds_dwordx4 v143, s[10:11]
	v_cvt_scalef32_pk_bf16_fp4 v98, v82, 1.0
	v_cvt_scalef32_pk_bf16_fp4 v99, v82, 1.0 op_sel:[1,0,0]
	v_cvt_scalef32_pk_bf16_fp4 v100, v82, 1.0 op_sel:[0,1,0]
	v_cvt_scalef32_pk_bf16_fp4 v101, v82, 1.0 op_sel:[1,1,0]
	v_cvt_scalef32_pk_bf16_fp4 v102, v83, 1.0
	v_cvt_scalef32_pk_bf16_fp4 v103, v83, 1.0 op_sel:[1,0,0]
	v_cvt_scalef32_pk_bf16_fp4 v104, v83, 1.0 op_sel:[0,1,0]
	v_cvt_scalef32_pk_bf16_fp4 v105, v83, 1.0 op_sel:[1,1,0]
	v_mfma_f32_16x16x32_bf16 v[122:125], v[34:37], v[98:101], 0
	v_cvt_scalef32_pk_bf16_fp4 v98, v84, 1.0
	v_cvt_scalef32_pk_bf16_fp4 v99, v84, 1.0 op_sel:[1,0,0]
	v_cvt_scalef32_pk_bf16_fp4 v100, v84, 1.0 op_sel:[0,1,0]
	v_cvt_scalef32_pk_bf16_fp4 v101, v84, 1.0 op_sel:[1,1,0]
	v_mfma_f32_16x16x32_bf16 v[122:125], v[38:41], v[102:105], v[122:125]
	v_cvt_scalef32_pk_bf16_fp4 v102, v85, 1.0
	v_cvt_scalef32_pk_bf16_fp4 v103, v85, 1.0 op_sel:[1,0,0]
	v_cvt_scalef32_pk_bf16_fp4 v104, v85, 1.0 op_sel:[0,1,0]
	v_cvt_scalef32_pk_bf16_fp4 v105, v85, 1.0 op_sel:[1,1,0]
	v_mfma_f32_16x16x32_bf16 v[122:125], v[42:45], v[98:101], v[122:125]
	v_cvt_scalef32_pk_bf16_fp4 v98, v86, 1.0
	v_cvt_scalef32_pk_bf16_fp4 v99, v86, 1.0 op_sel:[1,0,0]
	v_cvt_scalef32_pk_bf16_fp4 v100, v86, 1.0 op_sel:[0,1,0]
	v_cvt_scalef32_pk_bf16_fp4 v101, v86, 1.0 op_sel:[1,1,0]
	v_mfma_f32_16x16x32_bf16 v[122:125], v[46:49], v[102:105], v[122:125]
	v_cvt_scalef32_pk_bf16_fp4 v102, v87, 1.0
	v_cvt_scalef32_pk_bf16_fp4 v103, v87, 1.0 op_sel:[1,0,0]
	v_cvt_scalef32_pk_bf16_fp4 v104, v87, 1.0 op_sel:[0,1,0]
	v_cvt_scalef32_pk_bf16_fp4 v105, v87, 1.0 op_sel:[1,1,0]
	v_mfma_f32_16x16x32_bf16 v[122:125], v[50:53], v[98:101], v[122:125]
	v_cvt_scalef32_pk_bf16_fp4 v98, v88, 1.0
	v_cvt_scalef32_pk_bf16_fp4 v99, v88, 1.0 op_sel:[1,0,0]
	v_cvt_scalef32_pk_bf16_fp4 v100, v88, 1.0 op_sel:[0,1,0]
	v_cvt_scalef32_pk_bf16_fp4 v101, v88, 1.0 op_sel:[1,1,0]
	v_mfma_f32_16x16x32_bf16 v[122:125], v[54:57], v[102:105], v[122:125]
	v_cvt_scalef32_pk_bf16_fp4 v102, v89, 1.0
	v_cvt_scalef32_pk_bf16_fp4 v103, v89, 1.0 op_sel:[1,0,0]
	v_cvt_scalef32_pk_bf16_fp4 v104, v89, 1.0 op_sel:[0,1,0]
	v_cvt_scalef32_pk_bf16_fp4 v105, v89, 1.0 op_sel:[1,1,0]
	v_mfma_f32_16x16x32_bf16 v[122:125], v[58:61], v[98:101], v[122:125]
	v_mfma_f32_16x16x32_bf16 v[122:125], v[62:65], v[102:105], v[122:125]
	s_waitcnt vmcnt(15)
	ds_read_b128 v[82:85], v146 offset:12288
	ds_read_b128 v[86:89], v147 offset:12288
	s_waitcnt lgkmcnt(2)
	s_add_i32 m0, s38, 0x2800
	v_mad_u32_u16 v142, v68, v249, v144 op_sel:[1,0,0,0]
	global_load_lds_dwordx4 v142, s[10:11]
	s_add_i32 m0, s38, 0x2c00
	v_mad_u32_u16 v143, v72, v249, v145 op_sel:[1,0,0,0]
	global_load_lds_dwordx4 v143, s[10:11]
	v_cvt_scalef32_pk_bf16_fp4 v98, v90, 1.0
	v_cvt_scalef32_pk_bf16_fp4 v99, v90, 1.0 op_sel:[1,0,0]
	v_cvt_scalef32_pk_bf16_fp4 v100, v90, 1.0 op_sel:[0,1,0]
	v_cvt_scalef32_pk_bf16_fp4 v101, v90, 1.0 op_sel:[1,1,0]
	v_cvt_scalef32_pk_bf16_fp4 v102, v91, 1.0
	v_cvt_scalef32_pk_bf16_fp4 v103, v91, 1.0 op_sel:[1,0,0]
	v_cvt_scalef32_pk_bf16_fp4 v104, v91, 1.0 op_sel:[0,1,0]
	v_cvt_scalef32_pk_bf16_fp4 v105, v91, 1.0 op_sel:[1,1,0]
	v_mfma_f32_16x16x32_bf16 v[126:129], v[34:37], v[98:101], 0
	v_cvt_scalef32_pk_bf16_fp4 v98, v92, 1.0
	v_cvt_scalef32_pk_bf16_fp4 v99, v92, 1.0 op_sel:[1,0,0]
	v_cvt_scalef32_pk_bf16_fp4 v100, v92, 1.0 op_sel:[0,1,0]
	v_cvt_scalef32_pk_bf16_fp4 v101, v92, 1.0 op_sel:[1,1,0]
	v_mfma_f32_16x16x32_bf16 v[126:129], v[38:41], v[102:105], v[126:129]
	v_cvt_scalef32_pk_bf16_fp4 v102, v93, 1.0
	v_cvt_scalef32_pk_bf16_fp4 v103, v93, 1.0 op_sel:[1,0,0]
	v_cvt_scalef32_pk_bf16_fp4 v104, v93, 1.0 op_sel:[0,1,0]
	v_cvt_scalef32_pk_bf16_fp4 v105, v93, 1.0 op_sel:[1,1,0]
	v_mfma_f32_16x16x32_bf16 v[126:129], v[42:45], v[98:101], v[126:129]
	v_cvt_scalef32_pk_bf16_fp4 v98, v94, 1.0
	v_cvt_scalef32_pk_bf16_fp4 v99, v94, 1.0 op_sel:[1,0,0]
	v_cvt_scalef32_pk_bf16_fp4 v100, v94, 1.0 op_sel:[0,1,0]
	v_cvt_scalef32_pk_bf16_fp4 v101, v94, 1.0 op_sel:[1,1,0]
	v_mfma_f32_16x16x32_bf16 v[126:129], v[46:49], v[102:105], v[126:129]
	v_cvt_scalef32_pk_bf16_fp4 v102, v95, 1.0
	v_cvt_scalef32_pk_bf16_fp4 v103, v95, 1.0 op_sel:[1,0,0]
	v_cvt_scalef32_pk_bf16_fp4 v104, v95, 1.0 op_sel:[0,1,0]
	v_cvt_scalef32_pk_bf16_fp4 v105, v95, 1.0 op_sel:[1,1,0]
	v_mfma_f32_16x16x32_bf16 v[126:129], v[50:53], v[98:101], v[126:129]
	v_cvt_scalef32_pk_bf16_fp4 v98, v96, 1.0
	v_cvt_scalef32_pk_bf16_fp4 v99, v96, 1.0 op_sel:[1,0,0]
	v_cvt_scalef32_pk_bf16_fp4 v100, v96, 1.0 op_sel:[0,1,0]
	v_cvt_scalef32_pk_bf16_fp4 v101, v96, 1.0 op_sel:[1,1,0]
	v_mfma_f32_16x16x32_bf16 v[126:129], v[54:57], v[102:105], v[126:129]
	v_cvt_scalef32_pk_bf16_fp4 v102, v97, 1.0
	v_cvt_scalef32_pk_bf16_fp4 v103, v97, 1.0 op_sel:[1,0,0]
	v_cvt_scalef32_pk_bf16_fp4 v104, v97, 1.0 op_sel:[0,1,0]
	v_cvt_scalef32_pk_bf16_fp4 v105, v97, 1.0 op_sel:[1,1,0]
	v_mfma_f32_16x16x32_bf16 v[126:129], v[58:61], v[98:101], v[126:129]
	v_cvt_pk_bf16_f32 v139, v114, v118
	v_mfma_f32_16x16x32_bf16 v[126:129], v[62:65], v[102:105], v[126:129]
	s_waitcnt vmcnt(15)
	ds_read_b128 v[90:93], v146 offset:14336
	ds_read_b128 v[94:97], v147 offset:14336
	s_waitcnt lgkmcnt(2)
	s_add_i32 m0, s38, 0x3000
	v_mad_u32_u16 v142, v69, v249, v144
	global_load_lds_dwordx4 v142, s[10:11]
	s_add_i32 m0, s38, 0x3400
	v_mad_u32_u16 v143, v73, v249, v145
	global_load_lds_dwordx4 v143, s[10:11]
	v_cvt_scalef32_pk_bf16_fp4 v98, v82, 1.0
	v_cvt_scalef32_pk_bf16_fp4 v99, v82, 1.0 op_sel:[1,0,0]
	v_cvt_scalef32_pk_bf16_fp4 v100, v82, 1.0 op_sel:[0,1,0]
	v_cvt_scalef32_pk_bf16_fp4 v101, v82, 1.0 op_sel:[1,1,0]
	v_cvt_scalef32_pk_bf16_fp4 v102, v83, 1.0
	v_cvt_scalef32_pk_bf16_fp4 v103, v83, 1.0 op_sel:[1,0,0]
	v_cvt_scalef32_pk_bf16_fp4 v104, v83, 1.0 op_sel:[0,1,0]
	v_cvt_scalef32_pk_bf16_fp4 v105, v83, 1.0 op_sel:[1,1,0]
	v_mfma_f32_16x16x32_bf16 v[130:133], v[34:37], v[98:101], 0
	v_cvt_scalef32_pk_bf16_fp4 v98, v84, 1.0
	v_cvt_scalef32_pk_bf16_fp4 v99, v84, 1.0 op_sel:[1,0,0]
	v_cvt_scalef32_pk_bf16_fp4 v100, v84, 1.0 op_sel:[0,1,0]
	v_cvt_scalef32_pk_bf16_fp4 v101, v84, 1.0 op_sel:[1,1,0]
	v_mfma_f32_16x16x32_bf16 v[130:133], v[38:41], v[102:105], v[130:133]
	v_cvt_scalef32_pk_bf16_fp4 v102, v85, 1.0
	v_cvt_scalef32_pk_bf16_fp4 v103, v85, 1.0 op_sel:[1,0,0]
	v_cvt_scalef32_pk_bf16_fp4 v104, v85, 1.0 op_sel:[0,1,0]
	v_cvt_scalef32_pk_bf16_fp4 v105, v85, 1.0 op_sel:[1,1,0]
	v_mfma_f32_16x16x32_bf16 v[130:133], v[42:45], v[98:101], v[130:133]
	v_cvt_scalef32_pk_bf16_fp4 v98, v86, 1.0
	v_cvt_scalef32_pk_bf16_fp4 v99, v86, 1.0 op_sel:[1,0,0]
	v_cvt_scalef32_pk_bf16_fp4 v100, v86, 1.0 op_sel:[0,1,0]
	v_cvt_scalef32_pk_bf16_fp4 v101, v86, 1.0 op_sel:[1,1,0]
	v_mfma_f32_16x16x32_bf16 v[130:133], v[46:49], v[102:105], v[130:133]
	v_cvt_scalef32_pk_bf16_fp4 v102, v87, 1.0
	v_cvt_scalef32_pk_bf16_fp4 v103, v87, 1.0 op_sel:[1,0,0]
	v_cvt_scalef32_pk_bf16_fp4 v104, v87, 1.0 op_sel:[0,1,0]
	v_cvt_scalef32_pk_bf16_fp4 v105, v87, 1.0 op_sel:[1,1,0]
	v_mfma_f32_16x16x32_bf16 v[130:133], v[50:53], v[98:101], v[130:133]
	v_cvt_scalef32_pk_bf16_fp4 v98, v88, 1.0
	v_cvt_scalef32_pk_bf16_fp4 v99, v88, 1.0 op_sel:[1,0,0]
	v_cvt_scalef32_pk_bf16_fp4 v100, v88, 1.0 op_sel:[0,1,0]
	v_cvt_scalef32_pk_bf16_fp4 v101, v88, 1.0 op_sel:[1,1,0]
	v_mfma_f32_16x16x32_bf16 v[130:133], v[54:57], v[102:105], v[130:133]
	v_cvt_scalef32_pk_bf16_fp4 v102, v89, 1.0
	v_cvt_scalef32_pk_bf16_fp4 v103, v89, 1.0 op_sel:[1,0,0]
	v_cvt_scalef32_pk_bf16_fp4 v104, v89, 1.0 op_sel:[0,1,0]
	v_cvt_scalef32_pk_bf16_fp4 v105, v89, 1.0 op_sel:[1,1,0]
	v_mfma_f32_16x16x32_bf16 v[130:133], v[58:61], v[98:101], v[130:133]
	v_mfma_f32_16x16x32_bf16 v[130:133], v[62:65], v[102:105], v[130:133]
	s_waitcnt vmcnt(12)
	ds_read_b128 v[82:85], v146
	ds_read_b128 v[86:89], v147
	s_waitcnt lgkmcnt(2)
	s_add_i32 m0, s38, 0x3800
	v_mad_u32_u16 v142, v69, v249, v144 op_sel:[1,0,0,0]
	global_load_lds_dwordx4 v142, s[10:11]
	s_add_i32 m0, s38, 0x3c00
	v_mad_u32_u16 v143, v73, v249, v145 op_sel:[1,0,0,0]
	global_load_lds_dwordx4 v143, s[10:11]
	ds_read_b128 v[2:5], v148
	ds_read_b128 v[6:9], v148 offset:16
	ds_read_b128 v[10:13], v148 offset:32
	ds_read_b128 v[14:17], v148 offset:48
	ds_read_b128 v[18:21], v148 offset:256
	ds_read_b128 v[22:25], v148 offset:272
	ds_read_b128 v[26:29], v148 offset:288
	ds_read_b128 v[30:33], v148 offset:304
	ds_read_b128 v[74:77], v152 offset:256
	ds_read_b128 v[78:81], v152 offset:272
	v_cvt_scalef32_pk_bf16_fp4 v98, v90, 1.0
	v_cvt_scalef32_pk_bf16_fp4 v99, v90, 1.0 op_sel:[1,0,0]
	v_cvt_scalef32_pk_bf16_fp4 v100, v90, 1.0 op_sel:[0,1,0]
	v_cvt_scalef32_pk_bf16_fp4 v101, v90, 1.0 op_sel:[1,1,0]
	v_cvt_scalef32_pk_bf16_fp4 v102, v91, 1.0
	v_cvt_scalef32_pk_bf16_fp4 v103, v91, 1.0 op_sel:[1,0,0]
	v_cvt_scalef32_pk_bf16_fp4 v104, v91, 1.0 op_sel:[0,1,0]
	v_cvt_scalef32_pk_bf16_fp4 v105, v91, 1.0 op_sel:[1,1,0]
	v_mfma_f32_16x16x32_bf16 v[134:137], v[34:37], v[98:101], 0
	v_cvt_scalef32_pk_bf16_fp4 v98, v92, 1.0
	v_cvt_scalef32_pk_bf16_fp4 v99, v92, 1.0 op_sel:[1,0,0]
	v_cvt_scalef32_pk_bf16_fp4 v100, v92, 1.0 op_sel:[0,1,0]
	v_cvt_scalef32_pk_bf16_fp4 v101, v92, 1.0 op_sel:[1,1,0]
	v_mfma_f32_16x16x32_bf16 v[134:137], v[38:41], v[102:105], v[134:137]
	v_cvt_scalef32_pk_bf16_fp4 v102, v93, 1.0
	v_cvt_scalef32_pk_bf16_fp4 v103, v93, 1.0 op_sel:[1,0,0]
	v_cvt_scalef32_pk_bf16_fp4 v104, v93, 1.0 op_sel:[0,1,0]
	v_cvt_scalef32_pk_bf16_fp4 v105, v93, 1.0 op_sel:[1,1,0]
	v_mfma_f32_16x16x32_bf16 v[134:137], v[42:45], v[98:101], v[134:137]
	v_cvt_scalef32_pk_bf16_fp4 v98, v94, 1.0
	v_cvt_scalef32_pk_bf16_fp4 v99, v94, 1.0 op_sel:[1,0,0]
	v_cvt_scalef32_pk_bf16_fp4 v100, v94, 1.0 op_sel:[0,1,0]
	v_cvt_scalef32_pk_bf16_fp4 v101, v94, 1.0 op_sel:[1,1,0]
	v_mfma_f32_16x16x32_bf16 v[134:137], v[46:49], v[102:105], v[134:137]
	v_cvt_scalef32_pk_bf16_fp4 v102, v95, 1.0
	v_cvt_scalef32_pk_bf16_fp4 v103, v95, 1.0 op_sel:[1,0,0]
	v_cvt_scalef32_pk_bf16_fp4 v104, v95, 1.0 op_sel:[0,1,0]
	v_cvt_scalef32_pk_bf16_fp4 v105, v95, 1.0 op_sel:[1,1,0]
	v_mfma_f32_16x16x32_bf16 v[134:137], v[50:53], v[98:101], v[134:137]
	v_cvt_scalef32_pk_bf16_fp4 v98, v96, 1.0
	v_cvt_scalef32_pk_bf16_fp4 v99, v96, 1.0 op_sel:[1,0,0]
	v_cvt_scalef32_pk_bf16_fp4 v100, v96, 1.0 op_sel:[0,1,0]
	v_cvt_scalef32_pk_bf16_fp4 v101, v96, 1.0 op_sel:[1,1,0]
	v_mfma_f32_16x16x32_bf16 v[134:137], v[54:57], v[102:105], v[134:137]
	v_cvt_scalef32_pk_bf16_fp4 v102, v97, 1.0
	v_cvt_scalef32_pk_bf16_fp4 v103, v97, 1.0 op_sel:[1,0,0]
	v_cvt_scalef32_pk_bf16_fp4 v104, v97, 1.0 op_sel:[0,1,0]
	v_cvt_scalef32_pk_bf16_fp4 v105, v97, 1.0 op_sel:[1,1,0]
	v_mfma_f32_16x16x32_bf16 v[134:137], v[58:61], v[98:101], v[134:137]
	v_cvt_pk_bf16_f32 v140, v122, v126
	v_mfma_f32_16x16x32_bf16 v[134:137], v[62:65], v[102:105], v[134:137]
	s_nop 7
	s_nop 7
	v_cvt_pk_bf16_f32 v141, v130, v134
	s_mov_b64 exec, 0xffff
	global_store_dwordx4 v151, v[138:141], s[4:5]
	s_mov_b64 exec, -1
	v_add_u32_e32 v151, s42, v151
	s_add_i32 s34, s34, 2
	s_cmp_lt_u32 s34, 8
	s_cbranch_scc1 .Le1_loop
	s_cmp_lt_i32 s35, 0
	s_cbranch_scc1 .Le1_exit
	s_add_i32 s39, s39, s43
	s_add_i32 s39, s39, 7
	s_mov_b32 s34, 0
	s_branch .Le1_loop

.Le2w_first:
	s_mov_b64 exec, 1
	global_atomic_add v251, v211, v1, s[24:25] sc0
	s_mov_b64 exec, -1
	v_mov_b32_e32 v198, 0x80
	v_and_b32_e32 v233, 7, v0
	v_xor_b32_e32 v166, 0, v233
	v_lshlrev_b32_e32 v166, 4, v166
	v_xor_b32_e32 v167, 1, v233
	v_lshlrev_b32_e32 v167, 4, v167
	v_xor_b32_e32 v168, 2, v233
	v_lshlrev_b32_e32 v168, 4, v168
	v_xor_b32_e32 v169, 3, v233
	v_lshlrev_b32_e32 v169, 4, v169
	v_xor_b32_e32 v170, 4, v233
	v_lshlrev_b32_e32 v170, 4, v170
	v_xor_b32_e32 v171, 5, v233
	v_lshlrev_b32_e32 v171, 4, v171
	v_xor_b32_e32 v172, 6, v233
	v_lshlrev_b32_e32 v172, 4, v172
	v_xor_b32_e32 v173, 7, v233
	v_lshlrev_b32_e32 v173, 4, v173
	v_lshrrev_b32_e32 v234, 6, v0
	s_nop 0
	v_readfirstlane_b32 s38, v234
	s_lshl_b32 s38, s38, 14
	v_bfe_u32 v234, v0, 4, 2
	v_and_b32_e32 v196, 1, v234
	v_and_b32_e32 v197, 2, v234
	v_bfe_u32 v235, v0, 3, 1
	v_xor_b32_e32 v236, v235, v196
	v_lshl_add_u32 v236, v234, 1, v236
	v_lshl_add_u32 v236, v233, 3, v236
	v_lshlrev_b32_e32 v236, 7, v236
	v_lshl_add_u32 v236, v235, 3, v236
	v_add_u32_e32 v236, s38, v236
	v_xor_b32_e32 v237, 0, v233
	v_lshl_add_u32 v150, v237, 4, v236
	v_xor_b32_e32 v158, 8, v150
	v_xor_b32_e32 v237, 1, v233
	v_lshl_add_u32 v151, v237, 4, v236
	v_xor_b32_e32 v159, 8, v151
	v_xor_b32_e32 v237, 2, v233
	v_lshl_add_u32 v152, v237, 4, v236
	v_xor_b32_e32 v160, 8, v152
	v_xor_b32_e32 v237, 3, v233
	v_lshl_add_u32 v153, v237, 4, v236
	v_xor_b32_e32 v161, 8, v153
	v_xor_b32_e32 v237, 4, v233
	v_lshl_add_u32 v154, v237, 4, v236
	v_xor_b32_e32 v162, 8, v154
	v_xor_b32_e32 v237, 5, v233
	v_lshl_add_u32 v155, v237, 4, v236
	v_xor_b32_e32 v163, 8, v155
	v_xor_b32_e32 v237, 6, v233
	v_lshl_add_u32 v156, v237, 4, v236
	v_xor_b32_e32 v164, 8, v156
	v_xor_b32_e32 v237, 7, v233
	v_lshl_add_u32 v157, v237, 4, v236
	v_xor_b32_e32 v165, 8, v157
	s_lshr_b32 s99, s38, 4
	s_add_i32 s99, s99, 0x21000
	v_lshl_add_u32 v237, v196, 5, s99
	v_lshl_add_u32 v174, v234, 6, v237
	v_xor_b32_e32 v175, 32, v174
	s_lshr_b32 s99, s38, 5
	s_add_i32 s99, s99, 0x23000
	v_bfe_u32 v237, v0, 3, 3
	v_lshl_add_u32 v199, v237, 5, s99
	v_and_b32_e32 v237, 63, v0
	v_add_u32_e32 v237, s58, v237
	v_lshlrev_b32_e32 v184, 2, v237
	v_mov_b32_e32 v185, 0
	s_add_u32 s0, s56, 0xfffffef0
	s_addc_u32 s1, s57, -1
	s_lshl_b32 s42, s60, 3
	s_waitcnt vmcnt(0)
	v_readfirstlane_b32 s35, v251
	s_cmp_ge_i32 s35, s42
	s_cbranch_scc1 .LBB0_878
	s_lshr_b32 s99, s35, 3
	s_lshl_b32 s98, s99, 6
	s_and_b32 s99, s99, 0xffffff00
	s_add_i32 s99, s99, 0x100
	s_and_b64 s[2:3], s[30:31], exec
	s_cselect_b32 s99, 0, s99
	s_add_i32 s98, s98, s99
	s_and_b32 s99, s35, 7
	s_lshl_b32 s99, s99, 3
	s_add_i32 s98, s98, s99
	s_mov_b32 s39, s98
	s_lshl_b32 s99, s98, 8
	v_and_b32_e32 v235, 15, v0
	v_lshl_add_u32 v176, v235, 4, s99
	v_mov_b32_e32 v177, v176
	s_lshr_b32 s99, s38, 5
	s_add_i32 m0, s99, 0x23000
	s_mov_b64 exec, 0xffff
	global_load_lds_dwordx4 v176, s[22:23]
	s_mov_b64 exec, -1
	v_add_u32_e32 v176, 0x100, v176
	s_lshr_b32 s99, s38, 5
	s_add_i32 m0, s99, 0x23100
	s_mov_b64 exec, 0xffff
	global_load_lds_dwordx4 v176, s[22:23]
	s_mov_b64 exec, -1
	v_add_u32_e32 v176, 0x100, v176
	s_lshr_b32 s99, s38, 4
	s_add_i32 m0, s99, 0x21000
	s_mov_b64 exec, 0xffff
	global_load_lds_dwordx4 v177, s[0:1]
	s_mov_b64 exec, -1
	v_add_u32_e32 v177, 0x100, v177
	s_waitcnt vmcnt(0)
	ds_read_b128 v[98:101], v199
	ds_read_b128 v[102:105], v199 offset:16
	ds_read_b128 v[106:109], v199 offset:256
	ds_read_b128 v[110:113], v199 offset:272
	s_waitcnt lgkmcnt(0)
	s_add_i32 m0, s38, 0x0
	v_mad_u32_u16 v178, v98, v198, v166
	global_load_lds_dwordx4 v178, s[40:41]
	s_add_i32 m0, s38, 0x400
	v_mad_u32_u16 v179, v98, v198, v167 op_sel:[1,0,0,0]
	global_load_lds_dwordx4 v179, s[40:41]
	s_add_i32 m0, s38, 0x800
	v_mad_u32_u16 v178, v99, v198, v168
	global_load_lds_dwordx4 v178, s[40:41]
	s_add_i32 m0, s38, 0xc00
	v_mad_u32_u16 v179, v99, v198, v169 op_sel:[1,0,0,0]
	global_load_lds_dwordx4 v179, s[40:41]
	s_add_i32 m0, s38, 0x1000
	v_mad_u32_u16 v178, v100, v198, v170
	global_load_lds_dwordx4 v178, s[40:41]
	s_add_i32 m0, s38, 0x1400
	v_mad_u32_u16 v179, v100, v198, v171 op_sel:[1,0,0,0]
	global_load_lds_dwordx4 v179, s[40:41]
	s_add_i32 m0, s38, 0x1800
	v_mad_u32_u16 v178, v101, v198, v172
	global_load_lds_dwordx4 v178, s[40:41]
	s_add_i32 m0, s38, 0x1c00
	v_mad_u32_u16 v179, v101, v198, v173 op_sel:[1,0,0,0]
	global_load_lds_dwordx4 v179, s[40:41]
	s_add_i32 m0, s38, 0x2000
	v_mad_u32_u16 v178, v102, v198, v166
	global_load_lds_dwordx4 v178, s[40:41]
	s_add_i32 m0, s38, 0x2400
	v_mad_u32_u16 v179, v102, v198, v167 op_sel:[1,0,0,0]
	global_load_lds_dwordx4 v179, s[40:41]
	s_add_i32 m0, s38, 0x2800
	v_mad_u32_u16 v178, v103, v198, v168
	global_load_lds_dwordx4 v178, s[40:41]
	s_add_i32 m0, s38, 0x2c00
	v_mad_u32_u16 v179, v103, v198, v169 op_sel:[1,0,0,0]
	global_load_lds_dwordx4 v179, s[40:41]
	s_add_i32 m0, s38, 0x3000
	v_mad_u32_u16 v178, v104, v198, v170
	global_load_lds_dwordx4 v178, s[40:41]
	s_add_i32 m0, s38, 0x3400
	v_mad_u32_u16 v179, v104, v198, v171 op_sel:[1,0,0,0]
	global_load_lds_dwordx4 v179, s[40:41]
	s_add_i32 m0, s38, 0x3800
	v_mad_u32_u16 v178, v105, v198, v172
	global_load_lds_dwordx4 v178, s[40:41]
	s_add_i32 m0, s38, 0x3c00
	v_mad_u32_u16 v179, v105, v198, v173 op_sel:[1,0,0,0]
	global_load_lds_dwordx4 v179, s[40:41]
	v_mov_b32_e32 v194, s98
	v_mul_hi_i32 v186, v194, s69
	v_lshrrev_b32_e32 v187, 31, v186
	v_ashrrev_i32_e32 v186, 13, v186
	v_add_u32_e32 v187, v186, v187
	v_mul_i32_i24_e32 v190, 0xffffbf00, v187
	v_add_u32_e32 v186, v194, v190
	v_cmp_gt_i32_e32 vcc, s68, v186
	v_cmp_lt_i32_e64 s[2:3], s21, v186
	s_and_saveexec_b64 s[98:99], s[2:3]
	s_xor_b64 s[2:3], exec, s[98:99]
	v_lshl_add_u32 v186, v187, 14, v190
	v_add3_u32 v186, v194, v186, s88
	s_or_saveexec_b64 s[2:3], s[2:3]
	v_mov_b64_e32 v[188:189], s[18:19]
	s_xor_b64 exec, exec, s[2:3]
	v_lshlrev_b32_e32 v186, 8, v187
	v_add3_u32 v186, v190, v194, v186
	v_mov_b64_e32 v[188:189], s[72:73]
	s_or_b64 exec, exec, s[2:3]
	v_mul_i32_i24_e32 v187, 0x3000, v187
	v_cndmask_b32_e32 v190, v187, v223, vcc
	v_ashrrev_i32_e32 v191, 31, v190
	v_lshl_add_u64 v[190:191], v[190:191], 2, s[10:11]
	v_ashrrev_i32_e32 v187, 31, v186
	v_lshl_add_u64 v[192:193], v[190:191], 0, v[184:185]
	v_lshlrev_b64 v[186:187], 13, v[186:187]
	v_lshl_add_u64 v[186:187], v[188:189], 0, v[186:187]
	v_add_co_u32_e32 v192, vcc, s94, v192
	v_lshl_add_u64 v[180:181], v[186:187], 0, v[184:185]
	s_nop 0
	v_addc_co_u32_e32 v193, vcc, 0, v193, vcc
	global_load_dword v134, v[192:193], off
	global_load_dword v135, v[192:193], off offset:256
	global_load_dword v136, v[192:193], off offset:512
	global_load_dword v137, v[192:193], off offset:768
	s_mov_b32 s33, 0
	s_mov_b32 s43, 0
	s_waitcnt vmcnt(0)
	ds_read_b64_tr_b4 v[114:115], v150
	ds_read_b64_tr_b4 v[116:117], v158
	ds_read_b128 v[66:69], v174
	ds_read_b128 v[70:73], v174 offset:16
	ds_read_b128 v[74:77], v175
	ds_read_b128 v[78:81], v175 offset:16

.Le2_noprep:
	s_lshr_b32 s99, s38, 4
	s_add_i32 m0, s99, 0x21100
	s_mov_b64 exec, 0xffff
	global_load_lds_dwordx4 v177, s[0:1]
	s_mov_b64 exec, -1
	s_lshl_b32 s99, s43, 8
	s_cmp_eq_u32 s33, 6
	s_cselect_b32 s99, s99, 0x100
	v_add_u32_e32 v177, s99, v177
	s_lshr_b32 s99, s38, 5
	s_add_i32 m0, s99, 0x23000
	s_mov_b64 exec, 0xffff
	global_load_lds_dwordx4 v176, s[22:23]
	s_mov_b64 exec, -1
	v_add_u32_e32 v176, 0x100, v176
	global_load_dword v130, v[180:181], off
	global_load_dword v131, v[180:181], off offset:256
	global_load_dword v132, v[180:181], off offset:512
	global_load_dword v133, v[180:181], off offset:768
	ds_read_b64_tr_b4 v[118:119], v151
	ds_read_b64_tr_b4 v[120:121], v159
	s_waitcnt lgkmcnt(2)
	v_cvt_scalef32_pk_f16_fp4 v122, v114, 1.0
	v_cvt_scalef32_pk_f16_fp4 v123, v114, 1.0 op_sel:[1,0,0]
	v_cvt_scalef32_pk_f16_fp4 v124, v114, 1.0 op_sel:[0,1,0]
	v_cvt_scalef32_pk_f16_fp4 v125, v114, 1.0 op_sel:[1,1,0]
	v_cvt_scalef32_pk_f16_fp4 v126, v116, 1.0
	v_cvt_scalef32_pk_f16_fp4 v127, v116, 1.0 op_sel:[1,0,0]
	v_cvt_scalef32_pk_f16_fp4 v128, v116, 1.0 op_sel:[0,1,0]
	v_cvt_scalef32_pk_f16_fp4 v129, v116, 1.0 op_sel:[1,1,0]
	v_mfma_f32_16x16x32_f16 v[2:5], v[66:69], v[122:125], 0
	v_cvt_scalef32_pk_f16_fp4 v122, v117, 1.0
	v_cvt_scalef32_pk_f16_fp4 v123, v117, 1.0 op_sel:[1,0,0]
	v_cvt_scalef32_pk_f16_fp4 v124, v117, 1.0 op_sel:[0,1,0]
	v_cvt_scalef32_pk_f16_fp4 v125, v117, 1.0 op_sel:[1,1,0]
	v_mfma_f32_16x16x32_f16 v[6:9], v[66:69], v[126:129], 0
	v_cvt_scalef32_pk_f16_fp4 v126, v115, 1.0
	v_cvt_scalef32_pk_f16_fp4 v127, v115, 1.0 op_sel:[1,0,0]
	v_cvt_scalef32_pk_f16_fp4 v128, v115, 1.0 op_sel:[0,1,0]
	v_cvt_scalef32_pk_f16_fp4 v129, v115, 1.0 op_sel:[1,1,0]
	v_mfma_f32_16x16x32_f16 v[2:5], v[74:77], v[122:125], v[2:5]
	v_mfma_f32_16x16x32_f16 v[6:9], v[74:77], v[126:129], v[6:9]
	ds_read_b64_tr_b4 v[114:115], v152
	ds_read_b64_tr_b4 v[116:117], v160
	s_waitcnt lgkmcnt(2)
	v_cvt_scalef32_pk_f16_fp4 v122, v118, 1.0
	v_cvt_scalef32_pk_f16_fp4 v123, v118, 1.0 op_sel:[1,0,0]
	v_cvt_scalef32_pk_f16_fp4 v124, v118, 1.0 op_sel:[0,1,0]
	v_cvt_scalef32_pk_f16_fp4 v125, v118, 1.0 op_sel:[1,1,0]
	v_cvt_scalef32_pk_f16_fp4 v126, v120, 1.0
	v_cvt_scalef32_pk_f16_fp4 v127, v120, 1.0 op_sel:[1,0,0]
	v_cvt_scalef32_pk_f16_fp4 v128, v120, 1.0 op_sel:[0,1,0]
	v_cvt_scalef32_pk_f16_fp4 v129, v120, 1.0 op_sel:[1,1,0]
	v_mfma_f32_16x16x32_f16 v[10:13], v[66:69], v[122:125], 0
	v_cvt_scalef32_pk_f16_fp4 v122, v121, 1.0
	v_cvt_scalef32_pk_f16_fp4 v123, v121, 1.0 op_sel:[1,0,0]
	v_cvt_scalef32_pk_f16_fp4 v124, v121, 1.0 op_sel:[0,1,0]
	v_cvt_scalef32_pk_f16_fp4 v125, v121, 1.0 op_sel:[1,1,0]
	v_mfma_f32_16x16x32_f16 v[14:17], v[66:69], v[126:129], 0
	v_cvt_scalef32_pk_f16_fp4 v126, v119, 1.0
	v_cvt_scalef32_pk_f16_fp4 v127, v119, 1.0 op_sel:[1,0,0]
	v_cvt_scalef32_pk_f16_fp4 v128, v119, 1.0 op_sel:[0,1,0]
	v_cvt_scalef32_pk_f16_fp4 v129, v119, 1.0 op_sel:[1,1,0]
	v_mfma_f32_16x16x32_f16 v[10:13], v[74:77], v[122:125], v[10:13]
	v_mfma_f32_16x16x32_f16 v[14:17], v[74:77], v[126:129], v[14:17]
	ds_read_b64_tr_b4 v[118:119], v153
	ds_read_b64_tr_b4 v[120:121], v161
	s_waitcnt lgkmcnt(2)
	v_cvt_scalef32_pk_f16_fp4 v122, v114, 1.0
	v_cvt_scalef32_pk_f16_fp4 v123, v114, 1.0 op_sel:[1,0,0]
	v_cvt_scalef32_pk_f16_fp4 v124, v114, 1.0 op_sel:[0,1,0]
	v_cvt_scalef32_pk_f16_fp4 v125, v114, 1.0 op_sel:[1,1,0]
	v_cvt_scalef32_pk_f16_fp4 v126, v116, 1.0
	v_cvt_scalef32_pk_f16_fp4 v127, v116, 1.0 op_sel:[1,0,0]
	v_cvt_scalef32_pk_f16_fp4 v128, v116, 1.0 op_sel:[0,1,0]
	v_cvt_scalef32_pk_f16_fp4 v129, v116, 1.0 op_sel:[1,1,0]
	v_mfma_f32_16x16x32_f16 v[18:21], v[66:69], v[122:125], 0
	v_cvt_scalef32_pk_f16_fp4 v122, v117, 1.0
	v_cvt_scalef32_pk_f16_fp4 v123, v117, 1.0 op_sel:[1,0,0]
	v_cvt_scalef32_pk_f16_fp4 v124, v117, 1.0 op_sel:[0,1,0]
	v_cvt_scalef32_pk_f16_fp4 v125, v117, 1.0 op_sel:[1,1,0]
	v_mfma_f32_16x16x32_f16 v[22:25], v[66:69], v[126:129], 0
	v_cvt_scalef32_pk_f16_fp4 v126, v115, 1.0
	v_cvt_scalef32_pk_f16_fp4 v127, v115, 1.0 op_sel:[1,0,0]
	v_cvt_scalef32_pk_f16_fp4 v128, v115, 1.0 op_sel:[0,1,0]
	v_cvt_scalef32_pk_f16_fp4 v129, v115, 1.0 op_sel:[1,1,0]
	v_mfma_f32_16x16x32_f16 v[18:21], v[74:77], v[122:125], v[18:21]
	v_mfma_f32_16x16x32_f16 v[22:25], v[74:77], v[126:129], v[22:25]
	ds_read_b64_tr_b4 v[114:115], v154
	ds_read_b64_tr_b4 v[116:117], v162
	s_waitcnt lgkmcnt(2)
	v_cvt_scalef32_pk_f16_fp4 v122, v118, 1.0
	v_cvt_scalef32_pk_f16_fp4 v123, v118, 1.0 op_sel:[1,0,0]
	v_cvt_scalef32_pk_f16_fp4 v124, v118, 1.0 op_sel:[0,1,0]
	v_cvt_scalef32_pk_f16_fp4 v125, v118, 1.0 op_sel:[1,1,0]
	v_cvt_scalef32_pk_f16_fp4 v126, v120, 1.0
	v_cvt_scalef32_pk_f16_fp4 v127, v120, 1.0 op_sel:[1,0,0]
	v_cvt_scalef32_pk_f16_fp4 v128, v120, 1.0 op_sel:[0,1,0]
	v_cvt_scalef32_pk_f16_fp4 v129, v120, 1.0 op_sel:[1,1,0]
	v_mfma_f32_16x16x32_f16 v[26:29], v[66:69], v[122:125], 0
	v_cvt_scalef32_pk_f16_fp4 v122, v121, 1.0
	v_cvt_scalef32_pk_f16_fp4 v123, v121, 1.0 op_sel:[1,0,0]
	v_cvt_scalef32_pk_f16_fp4 v124, v121, 1.0 op_sel:[0,1,0]
	v_cvt_scalef32_pk_f16_fp4 v125, v121, 1.0 op_sel:[1,1,0]
	v_mfma_f32_16x16x32_f16 v[30:33], v[66:69], v[126:129], 0
	v_cvt_scalef32_pk_f16_fp4 v126, v119, 1.0
	v_cvt_scalef32_pk_f16_fp4 v127, v119, 1.0 op_sel:[1,0,0]
	v_cvt_scalef32_pk_f16_fp4 v128, v119, 1.0 op_sel:[0,1,0]
	v_cvt_scalef32_pk_f16_fp4 v129, v119, 1.0 op_sel:[1,1,0]
	v_mfma_f32_16x16x32_f16 v[26:29], v[74:77], v[122:125], v[26:29]
	v_mfma_f32_16x16x32_f16 v[30:33], v[74:77], v[126:129], v[30:33]
	ds_read_b64_tr_b4 v[118:119], v155
	ds_read_b64_tr_b4 v[120:121], v163
	s_waitcnt lgkmcnt(2)
	v_cvt_scalef32_pk_f16_fp4 v122, v114, 1.0
	v_cvt_scalef32_pk_f16_fp4 v123, v114, 1.0 op_sel:[1,0,0]
	v_cvt_scalef32_pk_f16_fp4 v124, v114, 1.0 op_sel:[0,1,0]
	v_cvt_scalef32_pk_f16_fp4 v125, v114, 1.0 op_sel:[1,1,0]
	v_cvt_scalef32_pk_f16_fp4 v126, v116, 1.0
	v_cvt_scalef32_pk_f16_fp4 v127, v116, 1.0 op_sel:[1,0,0]
	v_cvt_scalef32_pk_f16_fp4 v128, v116, 1.0 op_sel:[0,1,0]
	v_cvt_scalef32_pk_f16_fp4 v129, v116, 1.0 op_sel:[1,1,0]
	v_mfma_f32_16x16x32_f16 v[34:37], v[66:69], v[122:125], 0
	v_cvt_scalef32_pk_f16_fp4 v122, v117, 1.0
	v_cvt_scalef32_pk_f16_fp4 v123, v117, 1.0 op_sel:[1,0,0]
	v_cvt_scalef32_pk_f16_fp4 v124, v117, 1.0 op_sel:[0,1,0]
	v_cvt_scalef32_pk_f16_fp4 v125, v117, 1.0 op_sel:[1,1,0]
	v_mfma_f32_16x16x32_f16 v[38:41], v[66:69], v[126:129], 0
	v_cvt_scalef32_pk_f16_fp4 v126, v115, 1.0
	v_cvt_scalef32_pk_f16_fp4 v127, v115, 1.0 op_sel:[1,0,0]
	v_cvt_scalef32_pk_f16_fp4 v128, v115, 1.0 op_sel:[0,1,0]
	v_cvt_scalef32_pk_f16_fp4 v129, v115, 1.0 op_sel:[1,1,0]
	v_mfma_f32_16x16x32_f16 v[34:37], v[74:77], v[122:125], v[34:37]
	v_mfma_f32_16x16x32_f16 v[38:41], v[74:77], v[126:129], v[38:41]
	ds_read_b64_tr_b4 v[114:115], v156
	ds_read_b64_tr_b4 v[116:117], v164
	s_waitcnt lgkmcnt(2)
	v_cvt_scalef32_pk_f16_fp4 v122, v118, 1.0
	v_cvt_scalef32_pk_f16_fp4 v123, v118, 1.0 op_sel:[1,0,0]
	v_cvt_scalef32_pk_f16_fp4 v124, v118, 1.0 op_sel:[0,1,0]
	v_cvt_scalef32_pk_f16_fp4 v125, v118, 1.0 op_sel:[1,1,0]
	v_cvt_scalef32_pk_f16_fp4 v126, v120, 1.0
	v_cvt_scalef32_pk_f16_fp4 v127, v120, 1.0 op_sel:[1,0,0]
	v_cvt_scalef32_pk_f16_fp4 v128, v120, 1.0 op_sel:[0,1,0]
	v_cvt_scalef32_pk_f16_fp4 v129, v120, 1.0 op_sel:[1,1,0]
	v_mfma_f32_16x16x32_f16 v[42:45], v[66:69], v[122:125], 0
	v_cvt_scalef32_pk_f16_fp4 v122, v121, 1.0
	v_cvt_scalef32_pk_f16_fp4 v123, v121, 1.0 op_sel:[1,0,0]
	v_cvt_scalef32_pk_f16_fp4 v124, v121, 1.0 op_sel:[0,1,0]
	v_cvt_scalef32_pk_f16_fp4 v125, v121, 1.0 op_sel:[1,1,0]
	v_mfma_f32_16x16x32_f16 v[46:49], v[66:69], v[126:129], 0
	v_cvt_scalef32_pk_f16_fp4 v126, v119, 1.0
	v_cvt_scalef32_pk_f16_fp4 v127, v119, 1.0 op_sel:[1,0,0]
	v_cvt_scalef32_pk_f16_fp4 v128, v119, 1.0 op_sel:[0,1,0]
	v_cvt_scalef32_pk_f16_fp4 v129, v119, 1.0 op_sel:[1,1,0]
	v_mfma_f32_16x16x32_f16 v[42:45], v[74:77], v[122:125], v[42:45]
	v_mfma_f32_16x16x32_f16 v[46:49], v[74:77], v[126:129], v[46:49]
	ds_read_b64_tr_b4 v[118:119], v157
	ds_read_b64_tr_b4 v[120:121], v165
	s_waitcnt lgkmcnt(2)
	v_cvt_scalef32_pk_f16_fp4 v122, v114, 1.0
	v_cvt_scalef32_pk_f16_fp4 v123, v114, 1.0 op_sel:[1,0,0]
	v_cvt_scalef32_pk_f16_fp4 v124, v114, 1.0 op_sel:[0,1,0]
	v_cvt_scalef32_pk_f16_fp4 v125, v114, 1.0 op_sel:[1,1,0]
	v_cvt_scalef32_pk_f16_fp4 v126, v116, 1.0
	v_cvt_scalef32_pk_f16_fp4 v127, v116, 1.0 op_sel:[1,0,0]
	v_cvt_scalef32_pk_f16_fp4 v128, v116, 1.0 op_sel:[0,1,0]
	v_cvt_scalef32_pk_f16_fp4 v129, v116, 1.0 op_sel:[1,1,0]
	v_mfma_f32_16x16x32_f16 v[50:53], v[66:69], v[122:125], 0
	v_cvt_scalef32_pk_f16_fp4 v122, v117, 1.0
	v_cvt_scalef32_pk_f16_fp4 v123, v117, 1.0 op_sel:[1,0,0]
	v_cvt_scalef32_pk_f16_fp4 v124, v117, 1.0 op_sel:[0,1,0]
	v_cvt_scalef32_pk_f16_fp4 v125, v117, 1.0 op_sel:[1,1,0]
	v_mfma_f32_16x16x32_f16 v[54:57], v[66:69], v[126:129], 0
	v_cvt_scalef32_pk_f16_fp4 v126, v115, 1.0
	v_cvt_scalef32_pk_f16_fp4 v127, v115, 1.0 op_sel:[1,0,0]
	v_cvt_scalef32_pk_f16_fp4 v128, v115, 1.0 op_sel:[0,1,0]
	v_cvt_scalef32_pk_f16_fp4 v129, v115, 1.0 op_sel:[1,1,0]
	v_mfma_f32_16x16x32_f16 v[50:53], v[74:77], v[122:125], v[50:53]
	v_mfma_f32_16x16x32_f16 v[54:57], v[74:77], v[126:129], v[54:57]
	s_waitcnt vmcnt(10)
	ds_read_b64_tr_b4 v[114:115], v150 offset:8192
	ds_read_b64_tr_b4 v[116:117], v158 offset:8192
	s_waitcnt lgkmcnt(2)
	s_add_i32 m0, s38, 0x0
	v_mad_u32_u16 v178, v106, v198, v166
	global_load_lds_dwordx4 v178, s[40:41]
	s_add_i32 m0, s38, 0x400
	v_mad_u32_u16 v179, v106, v198, v167 op_sel:[1,0,0,0]
	global_load_lds_dwordx4 v179, s[40:41]
	s_add_i32 m0, s38, 0x800
	v_mad_u32_u16 v178, v107, v198, v168
	global_load_lds_dwordx4 v178, s[40:41]
	s_add_i32 m0, s38, 0xc00
	v_mad_u32_u16 v179, v107, v198, v169 op_sel:[1,0,0,0]
	global_load_lds_dwordx4 v179, s[40:41]
	s_add_i32 m0, s38, 0x1000
	v_mad_u32_u16 v178, v108, v198, v170
	global_load_lds_dwordx4 v178, s[40:41]
	s_add_i32 m0, s38, 0x1400
	v_mad_u32_u16 v179, v108, v198, v171 op_sel:[1,0,0,0]
	global_load_lds_dwordx4 v179, s[40:41]
	s_add_i32 m0, s38, 0x1800
	v_mad_u32_u16 v178, v109, v198, v172
	global_load_lds_dwordx4 v178, s[40:41]
	s_add_i32 m0, s38, 0x1c00
	v_mad_u32_u16 v179, v109, v198, v173 op_sel:[1,0,0,0]
	global_load_lds_dwordx4 v179, s[40:41]
	v_cvt_scalef32_pk_f16_fp4 v122, v118, 1.0
	v_cvt_scalef32_pk_f16_fp4 v123, v118, 1.0 op_sel:[1,0,0]
	v_cvt_scalef32_pk_f16_fp4 v124, v118, 1.0 op_sel:[0,1,0]
	v_cvt_scalef32_pk_f16_fp4 v125, v118, 1.0 op_sel:[1,1,0]
	v_cvt_scalef32_pk_f16_fp4 v126, v120, 1.0
	v_cvt_scalef32_pk_f16_fp4 v127, v120, 1.0 op_sel:[1,0,0]
	v_cvt_scalef32_pk_f16_fp4 v128, v120, 1.0 op_sel:[0,1,0]
	v_cvt_scalef32_pk_f16_fp4 v129, v120, 1.0 op_sel:[1,1,0]
	v_mfma_f32_16x16x32_f16 v[58:61], v[66:69], v[122:125], 0
	v_cvt_scalef32_pk_f16_fp4 v122, v121, 1.0
	v_cvt_scalef32_pk_f16_fp4 v123, v121, 1.0 op_sel:[1,0,0]
	v_cvt_scalef32_pk_f16_fp4 v124, v121, 1.0 op_sel:[0,1,0]
	v_cvt_scalef32_pk_f16_fp4 v125, v121, 1.0 op_sel:[1,1,0]
	v_mfma_f32_16x16x32_f16 v[62:65], v[66:69], v[126:129], 0
	v_cvt_scalef32_pk_f16_fp4 v126, v119, 1.0
	v_cvt_scalef32_pk_f16_fp4 v127, v119, 1.0 op_sel:[1,0,0]
	v_cvt_scalef32_pk_f16_fp4 v128, v119, 1.0 op_sel:[0,1,0]
	v_cvt_scalef32_pk_f16_fp4 v129, v119, 1.0 op_sel:[1,1,0]
	v_mfma_f32_16x16x32_f16 v[58:61], v[74:77], v[122:125], v[58:61]
	v_mfma_f32_16x16x32_f16 v[62:65], v[74:77], v[126:129], v[62:65]
	ds_read_b64_tr_b4 v[118:119], v151 offset:8192
	ds_read_b64_tr_b4 v[120:121], v159 offset:8192
	s_waitcnt lgkmcnt(2)
	v_cvt_scalef32_pk_f16_fp4 v122, v114, 1.0
	v_cvt_scalef32_pk_f16_fp4 v123, v114, 1.0 op_sel:[1,0,0]
	v_cvt_scalef32_pk_f16_fp4 v124, v114, 1.0 op_sel:[0,1,0]
	v_cvt_scalef32_pk_f16_fp4 v125, v114, 1.0 op_sel:[1,1,0]
	v_cvt_scalef32_pk_f16_fp4 v126, v116, 1.0
	v_cvt_scalef32_pk_f16_fp4 v127, v116, 1.0 op_sel:[1,0,0]
	v_cvt_scalef32_pk_f16_fp4 v128, v116, 1.0 op_sel:[0,1,0]
	v_cvt_scalef32_pk_f16_fp4 v129, v116, 1.0 op_sel:[1,1,0]
	v_mfma_f32_16x16x32_f16 v[2:5], v[70:73], v[122:125], v[2:5]
	v_cvt_scalef32_pk_f16_fp4 v122, v117, 1.0
	v_cvt_scalef32_pk_f16_fp4 v123, v117, 1.0 op_sel:[1,0,0]
	v_cvt_scalef32_pk_f16_fp4 v124, v117, 1.0 op_sel:[0,1,0]
	v_cvt_scalef32_pk_f16_fp4 v125, v117, 1.0 op_sel:[1,1,0]
	v_mfma_f32_16x16x32_f16 v[6:9], v[70:73], v[126:129], v[6:9]
	v_cvt_scalef32_pk_f16_fp4 v126, v115, 1.0
	v_cvt_scalef32_pk_f16_fp4 v127, v115, 1.0 op_sel:[1,0,0]
	v_cvt_scalef32_pk_f16_fp4 v128, v115, 1.0 op_sel:[0,1,0]
	v_cvt_scalef32_pk_f16_fp4 v129, v115, 1.0 op_sel:[1,1,0]
	v_mfma_f32_16x16x32_f16 v[2:5], v[78:81], v[122:125], v[2:5]
	v_mfma_f32_16x16x32_f16 v[6:9], v[78:81], v[126:129], v[6:9]
	ds_read_b64_tr_b4 v[114:115], v152 offset:8192
	ds_read_b64_tr_b4 v[116:117], v160 offset:8192
	s_waitcnt lgkmcnt(2)
	v_cvt_scalef32_pk_f16_fp4 v122, v118, 1.0
	v_cvt_scalef32_pk_f16_fp4 v123, v118, 1.0 op_sel:[1,0,0]
	v_cvt_scalef32_pk_f16_fp4 v124, v118, 1.0 op_sel:[0,1,0]
	v_cvt_scalef32_pk_f16_fp4 v125, v118, 1.0 op_sel:[1,1,0]
	v_cvt_scalef32_pk_f16_fp4 v126, v120, 1.0
	v_cvt_scalef32_pk_f16_fp4 v127, v120, 1.0 op_sel:[1,0,0]
	v_cvt_scalef32_pk_f16_fp4 v128, v120, 1.0 op_sel:[0,1,0]
	v_cvt_scalef32_pk_f16_fp4 v129, v120, 1.0 op_sel:[1,1,0]
	v_mfma_f32_16x16x32_f16 v[10:13], v[70:73], v[122:125], v[10:13]
	v_cvt_scalef32_pk_f16_fp4 v122, v121, 1.0
	v_cvt_scalef32_pk_f16_fp4 v123, v121, 1.0 op_sel:[1,0,0]
	v_cvt_scalef32_pk_f16_fp4 v124, v121, 1.0 op_sel:[0,1,0]
	v_cvt_scalef32_pk_f16_fp4 v125, v121, 1.0 op_sel:[1,1,0]
	v_mfma_f32_16x16x32_f16 v[14:17], v[70:73], v[126:129], v[14:17]
	v_cvt_scalef32_pk_f16_fp4 v126, v119, 1.0
	v_cvt_scalef32_pk_f16_fp4 v127, v119, 1.0 op_sel:[1,0,0]
	v_cvt_scalef32_pk_f16_fp4 v128, v119, 1.0 op_sel:[0,1,0]
	v_cvt_scalef32_pk_f16_fp4 v129, v119, 1.0 op_sel:[1,1,0]
	v_mfma_f32_16x16x32_f16 v[10:13], v[78:81], v[122:125], v[10:13]
	v_mfma_f32_16x16x32_f16 v[14:17], v[78:81], v[126:129], v[14:17]
	ds_read_b64_tr_b4 v[118:119], v153 offset:8192
	ds_read_b64_tr_b4 v[120:121], v161 offset:8192
	s_waitcnt lgkmcnt(2)
	v_cvt_scalef32_pk_f16_fp4 v122, v114, 1.0
	v_cvt_scalef32_pk_f16_fp4 v123, v114, 1.0 op_sel:[1,0,0]
	v_cvt_scalef32_pk_f16_fp4 v124, v114, 1.0 op_sel:[0,1,0]
	v_cvt_scalef32_pk_f16_fp4 v125, v114, 1.0 op_sel:[1,1,0]
	v_cvt_scalef32_pk_f16_fp4 v126, v116, 1.0
	v_cvt_scalef32_pk_f16_fp4 v127, v116, 1.0 op_sel:[1,0,0]
	v_cvt_scalef32_pk_f16_fp4 v128, v116, 1.0 op_sel:[0,1,0]
	v_cvt_scalef32_pk_f16_fp4 v129, v116, 1.0 op_sel:[1,1,0]
	v_mfma_f32_16x16x32_f16 v[18:21], v[70:73], v[122:125], v[18:21]
	v_cvt_scalef32_pk_f16_fp4 v122, v117, 1.0
	v_cvt_scalef32_pk_f16_fp4 v123, v117, 1.0 op_sel:[1,0,0]
	v_cvt_scalef32_pk_f16_fp4 v124, v117, 1.0 op_sel:[0,1,0]
	v_cvt_scalef32_pk_f16_fp4 v125, v117, 1.0 op_sel:[1,1,0]
	v_mfma_f32_16x16x32_f16 v[22:25], v[70:73], v[126:129], v[22:25]
	v_cvt_scalef32_pk_f16_fp4 v126, v115, 1.0
	v_cvt_scalef32_pk_f16_fp4 v127, v115, 1.0 op_sel:[1,0,0]
	v_cvt_scalef32_pk_f16_fp4 v128, v115, 1.0 op_sel:[0,1,0]
	v_cvt_scalef32_pk_f16_fp4 v129, v115, 1.0 op_sel:[1,1,0]
	v_mfma_f32_16x16x32_f16 v[18:21], v[78:81], v[122:125], v[18:21]
	v_mfma_f32_16x16x32_f16 v[22:25], v[78:81], v[126:129], v[22:25]
	ds_read_b64_tr_b4 v[114:115], v154 offset:8192
	ds_read_b64_tr_b4 v[116:117], v162 offset:8192
	s_waitcnt lgkmcnt(2)
	v_cvt_scalef32_pk_f16_fp4 v122, v118, 1.0
	v_cvt_scalef32_pk_f16_fp4 v123, v118, 1.0 op_sel:[1,0,0]
	v_cvt_scalef32_pk_f16_fp4 v124, v118, 1.0 op_sel:[0,1,0]
	v_cvt_scalef32_pk_f16_fp4 v125, v118, 1.0 op_sel:[1,1,0]
	v_cvt_scalef32_pk_f16_fp4 v126, v120, 1.0
	v_cvt_scalef32_pk_f16_fp4 v127, v120, 1.0 op_sel:[1,0,0]
	v_cvt_scalef32_pk_f16_fp4 v128, v120, 1.0 op_sel:[0,1,0]
	v_cvt_scalef32_pk_f16_fp4 v129, v120, 1.0 op_sel:[1,1,0]
	v_mfma_f32_16x16x32_f16 v[26:29], v[70:73], v[122:125], v[26:29]
	v_cvt_scalef32_pk_f16_fp4 v122, v121, 1.0
	v_cvt_scalef32_pk_f16_fp4 v123, v121, 1.0 op_sel:[1,0,0]
	v_cvt_scalef32_pk_f16_fp4 v124, v121, 1.0 op_sel:[0,1,0]
	v_cvt_scalef32_pk_f16_fp4 v125, v121, 1.0 op_sel:[1,1,0]
	v_mfma_f32_16x16x32_f16 v[30:33], v[70:73], v[126:129], v[30:33]
	v_cvt_scalef32_pk_f16_fp4 v126, v119, 1.0
	v_cvt_scalef32_pk_f16_fp4 v127, v119, 1.0 op_sel:[1,0,0]
	v_cvt_scalef32_pk_f16_fp4 v128, v119, 1.0 op_sel:[0,1,0]
	v_cvt_scalef32_pk_f16_fp4 v129, v119, 1.0 op_sel:[1,1,0]
	v_mfma_f32_16x16x32_f16 v[26:29], v[78:81], v[122:125], v[26:29]
	v_mfma_f32_16x16x32_f16 v[30:33], v[78:81], v[126:129], v[30:33]
	ds_read_b64_tr_b4 v[118:119], v155 offset:8192
	ds_read_b64_tr_b4 v[120:121], v163 offset:8192
	s_waitcnt lgkmcnt(2)
	v_cvt_scalef32_pk_f16_fp4 v122, v114, 1.0
	v_cvt_scalef32_pk_f16_fp4 v123, v114, 1.0 op_sel:[1,0,0]
	v_cvt_scalef32_pk_f16_fp4 v124, v114, 1.0 op_sel:[0,1,0]
	v_cvt_scalef32_pk_f16_fp4 v125, v114, 1.0 op_sel:[1,1,0]
	v_cvt_scalef32_pk_f16_fp4 v126, v116, 1.0
	v_cvt_scalef32_pk_f16_fp4 v127, v116, 1.0 op_sel:[1,0,0]
	v_cvt_scalef32_pk_f16_fp4 v128, v116, 1.0 op_sel:[0,1,0]
	v_cvt_scalef32_pk_f16_fp4 v129, v116, 1.0 op_sel:[1,1,0]
	v_mfma_f32_16x16x32_f16 v[34:37], v[70:73], v[122:125], v[34:37]
	v_cvt_scalef32_pk_f16_fp4 v122, v117, 1.0
	v_cvt_scalef32_pk_f16_fp4 v123, v117, 1.0 op_sel:[1,0,0]
	v_cvt_scalef32_pk_f16_fp4 v124, v117, 1.0 op_sel:[0,1,0]
	v_cvt_scalef32_pk_f16_fp4 v125, v117, 1.0 op_sel:[1,1,0]
	v_mfma_f32_16x16x32_f16 v[38:41], v[70:73], v[126:129], v[38:41]
	v_cvt_scalef32_pk_f16_fp4 v126, v115, 1.0
	v_cvt_scalef32_pk_f16_fp4 v127, v115, 1.0 op_sel:[1,0,0]
	v_cvt_scalef32_pk_f16_fp4 v128, v115, 1.0 op_sel:[0,1,0]
	v_cvt_scalef32_pk_f16_fp4 v129, v115, 1.0 op_sel:[1,1,0]
	v_mfma_f32_16x16x32_f16 v[34:37], v[78:81], v[122:125], v[34:37]
	v_mfma_f32_16x16x32_f16 v[38:41], v[78:81], v[126:129], v[38:41]
	ds_read_b64_tr_b4 v[114:115], v156 offset:8192
	ds_read_b64_tr_b4 v[116:117], v164 offset:8192
	s_waitcnt lgkmcnt(2)
	v_cvt_scalef32_pk_f16_fp4 v122, v118, 1.0
	v_cvt_scalef32_pk_f16_fp4 v123, v118, 1.0 op_sel:[1,0,0]
	v_cvt_scalef32_pk_f16_fp4 v124, v118, 1.0 op_sel:[0,1,0]
	v_cvt_scalef32_pk_f16_fp4 v125, v118, 1.0 op_sel:[1,1,0]
	v_cvt_scalef32_pk_f16_fp4 v126, v120, 1.0
	v_cvt_scalef32_pk_f16_fp4 v127, v120, 1.0 op_sel:[1,0,0]
	v_cvt_scalef32_pk_f16_fp4 v128, v120, 1.0 op_sel:[0,1,0]
	v_cvt_scalef32_pk_f16_fp4 v129, v120, 1.0 op_sel:[1,1,0]
	v_mfma_f32_16x16x32_f16 v[42:45], v[70:73], v[122:125], v[42:45]
	v_cvt_scalef32_pk_f16_fp4 v122, v121, 1.0
	v_cvt_scalef32_pk_f16_fp4 v123, v121, 1.0 op_sel:[1,0,0]
	v_cvt_scalef32_pk_f16_fp4 v124, v121, 1.0 op_sel:[0,1,0]
	v_cvt_scalef32_pk_f16_fp4 v125, v121, 1.0 op_sel:[1,1,0]
	v_mfma_f32_16x16x32_f16 v[46:49], v[70:73], v[126:129], v[46:49]
	v_cvt_scalef32_pk_f16_fp4 v126, v119, 1.0
	v_cvt_scalef32_pk_f16_fp4 v127, v119, 1.0 op_sel:[1,0,0]
	v_cvt_scalef32_pk_f16_fp4 v128, v119, 1.0 op_sel:[0,1,0]
	v_cvt_scalef32_pk_f16_fp4 v129, v119, 1.0 op_sel:[1,1,0]
	v_mfma_f32_16x16x32_f16 v[42:45], v[78:81], v[122:125], v[42:45]
	v_mfma_f32_16x16x32_f16 v[46:49], v[78:81], v[126:129], v[46:49]
	ds_read_b64_tr_b4 v[118:119], v157 offset:8192
	ds_read_b64_tr_b4 v[120:121], v165 offset:8192
	s_waitcnt lgkmcnt(2)
	v_cvt_scalef32_pk_f16_fp4 v122, v114, 1.0
	v_cvt_scalef32_pk_f16_fp4 v123, v114, 1.0 op_sel:[1,0,0]
	v_cvt_scalef32_pk_f16_fp4 v124, v114, 1.0 op_sel:[0,1,0]
	v_cvt_scalef32_pk_f16_fp4 v125, v114, 1.0 op_sel:[1,1,0]
	v_cvt_scalef32_pk_f16_fp4 v126, v116, 1.0
	v_cvt_scalef32_pk_f16_fp4 v127, v116, 1.0 op_sel:[1,0,0]
	v_cvt_scalef32_pk_f16_fp4 v128, v116, 1.0 op_sel:[0,1,0]
	v_cvt_scalef32_pk_f16_fp4 v129, v116, 1.0 op_sel:[1,1,0]
	v_mfma_f32_16x16x32_f16 v[50:53], v[70:73], v[122:125], v[50:53]
	v_cvt_scalef32_pk_f16_fp4 v122, v117, 1.0
	v_cvt_scalef32_pk_f16_fp4 v123, v117, 1.0 op_sel:[1,0,0]
	v_cvt_scalef32_pk_f16_fp4 v124, v117, 1.0 op_sel:[0,1,0]
	v_cvt_scalef32_pk_f16_fp4 v125, v117, 1.0 op_sel:[1,1,0]
	v_mfma_f32_16x16x32_f16 v[54:57], v[70:73], v[126:129], v[54:57]
	v_cvt_scalef32_pk_f16_fp4 v126, v115, 1.0
	v_cvt_scalef32_pk_f16_fp4 v127, v115, 1.0 op_sel:[1,0,0]
	v_cvt_scalef32_pk_f16_fp4 v128, v115, 1.0 op_sel:[0,1,0]
	v_cvt_scalef32_pk_f16_fp4 v129, v115, 1.0 op_sel:[1,1,0]
	v_mfma_f32_16x16x32_f16 v[50:53], v[78:81], v[122:125], v[50:53]
	v_mfma_f32_16x16x32_f16 v[54:57], v[78:81], v[126:129], v[54:57]
	s_waitcnt vmcnt(0)
	ds_read_b64_tr_b4 v[114:115], v150
	ds_read_b64_tr_b4 v[116:117], v158
	s_waitcnt lgkmcnt(2)
	s_add_i32 m0, s38, 0x2000
	v_mad_u32_u16 v178, v110, v198, v166
	global_load_lds_dwordx4 v178, s[40:41]
	s_add_i32 m0, s38, 0x2400
	v_mad_u32_u16 v179, v110, v198, v167 op_sel:[1,0,0,0]
	global_load_lds_dwordx4 v179, s[40:41]
	s_add_i32 m0, s38, 0x2800
	v_mad_u32_u16 v178, v111, v198, v168
	global_load_lds_dwordx4 v178, s[40:41]
	s_add_i32 m0, s38, 0x2c00
	v_mad_u32_u16 v179, v111, v198, v169 op_sel:[1,0,0,0]
	global_load_lds_dwordx4 v179, s[40:41]
	s_add_i32 m0, s38, 0x3000
	v_mad_u32_u16 v178, v112, v198, v170
	global_load_lds_dwordx4 v178, s[40:41]
	s_add_i32 m0, s38, 0x3400
	v_mad_u32_u16 v179, v112, v198, v171 op_sel:[1,0,0,0]
	global_load_lds_dwordx4 v179, s[40:41]
	s_add_i32 m0, s38, 0x3800
	v_mad_u32_u16 v178, v113, v198, v172
	global_load_lds_dwordx4 v178, s[40:41]
	s_add_i32 m0, s38, 0x3c00
	v_mad_u32_u16 v179, v113, v198, v173 op_sel:[1,0,0,0]
	global_load_lds_dwordx4 v179, s[40:41]
	ds_read_b128 v[82:85], v174 offset:256
	ds_read_b128 v[86:89], v174 offset:272
	ds_read_b128 v[90:93], v175 offset:256
	ds_read_b128 v[94:97], v175 offset:272
	ds_read_b128 v[98:101], v199
	ds_read_b128 v[102:105], v199 offset:16
	v_cvt_scalef32_pk_f16_fp4 v122, v118, 1.0
	v_cvt_scalef32_pk_f16_fp4 v123, v118, 1.0 op_sel:[1,0,0]
	v_cvt_scalef32_pk_f16_fp4 v124, v118, 1.0 op_sel:[0,1,0]
	v_cvt_scalef32_pk_f16_fp4 v125, v118, 1.0 op_sel:[1,1,0]
	v_cvt_scalef32_pk_f16_fp4 v126, v120, 1.0
	v_cvt_scalef32_pk_f16_fp4 v127, v120, 1.0 op_sel:[1,0,0]
	v_cvt_scalef32_pk_f16_fp4 v128, v120, 1.0 op_sel:[0,1,0]
	v_cvt_scalef32_pk_f16_fp4 v129, v120, 1.0 op_sel:[1,1,0]
	v_mfma_f32_16x16x32_f16 v[58:61], v[70:73], v[122:125], v[58:61]
	v_cvt_scalef32_pk_f16_fp4 v122, v121, 1.0
	v_cvt_scalef32_pk_f16_fp4 v123, v121, 1.0 op_sel:[1,0,0]
	v_cvt_scalef32_pk_f16_fp4 v124, v121, 1.0 op_sel:[0,1,0]
	v_cvt_scalef32_pk_f16_fp4 v125, v121, 1.0 op_sel:[1,1,0]
	v_mfma_f32_16x16x32_f16 v[62:65], v[70:73], v[126:129], v[62:65]
	v_cvt_scalef32_pk_f16_fp4 v126, v119, 1.0
	v_cvt_scalef32_pk_f16_fp4 v127, v119, 1.0 op_sel:[1,0,0]
	v_cvt_scalef32_pk_f16_fp4 v128, v119, 1.0 op_sel:[0,1,0]
	v_cvt_scalef32_pk_f16_fp4 v129, v119, 1.0 op_sel:[1,1,0]
	v_mfma_f32_16x16x32_f16 v[58:61], v[78:81], v[122:125], v[58:61]
	v_mfma_f32_16x16x32_f16 v[62:65], v[78:81], v[126:129], v[62:65]
	s_nop 7
	s_nop 7
	v_cmp_ne_u32_e32 vcc, 0, v196
	v_cndmask_b32_e32 v146, v2, v6, vcc
	v_cndmask_b32_e32 v142, v10, v14, vcc
	v_cndmask_b32_e32 v147, v18, v22, vcc
	v_cndmask_b32_e32 v143, v26, v30, vcc
	v_cndmask_b32_e32 v148, v34, v38, vcc
	v_cndmask_b32_e32 v144, v42, v46, vcc
	v_cndmask_b32_e32 v149, v50, v54, vcc
	v_cndmask_b32_e32 v145, v58, v62, vcc
	v_cmp_ne_u32_e32 vcc, 0, v197
	v_cndmask_b32_e32 v146, v146, v142, vcc
	v_cndmask_b32_e32 v147, v147, v143, vcc
	v_cndmask_b32_e32 v148, v148, v144, vcc
	v_cndmask_b32_e32 v149, v149, v145, vcc
	v_fma_f32 v142, v134, v146, v130
	v_fma_f32 v143, v135, v147, v131
	v_fma_f32 v144, v136, v148, v132
	v_fma_f32 v145, v137, v149, v133
	global_store_dword v[180:181], v142, off
	global_store_dword v[180:181], v143, off offset:256
	global_store_dword v[180:181], v144, off offset:512
	global_store_dword v[180:181], v145, off offset:768
	v_lshl_add_u64 v[180:181], v[180:181], 0, s[48:49]
	s_lshr_b32 s99, s38, 4
	s_add_i32 m0, s99, 0x21000
	s_mov_b64 exec, 0xffff
	global_load_lds_dwordx4 v177, s[0:1]
	s_mov_b64 exec, -1
	v_add_u32_e32 v177, 0x100, v177
	s_lshr_b32 s99, s38, 5
	s_add_i32 m0, s99, 0x23100
	s_mov_b64 exec, 0xffff
	global_load_lds_dwordx4 v176, s[22:23]
	s_mov_b64 exec, -1
	s_lshl_b32 s99, s43, 8
	s_cmp_eq_u32 s33, 4
	s_cselect_b32 s99, s99, 0x100
	v_add_u32_e32 v176, s99, v176
	global_load_dword v130, v[180:181], off
	global_load_dword v131, v[180:181], off offset:256
	global_load_dword v132, v[180:181], off offset:512
	global_load_dword v133, v[180:181], off offset:768
	ds_read_b64_tr_b4 v[118:119], v151
	ds_read_b64_tr_b4 v[120:121], v159
	s_waitcnt lgkmcnt(2)
	v_cvt_scalef32_pk_f16_fp4 v122, v114, 1.0
	v_cvt_scalef32_pk_f16_fp4 v123, v114, 1.0 op_sel:[1,0,0]
	v_cvt_scalef32_pk_f16_fp4 v124, v114, 1.0 op_sel:[0,1,0]
	v_cvt_scalef32_pk_f16_fp4 v125, v114, 1.0 op_sel:[1,1,0]
	v_cvt_scalef32_pk_f16_fp4 v126, v116, 1.0
	v_cvt_scalef32_pk_f16_fp4 v127, v116, 1.0 op_sel:[1,0,0]
	v_cvt_scalef32_pk_f16_fp4 v128, v116, 1.0 op_sel:[0,1,0]
	v_cvt_scalef32_pk_f16_fp4 v129, v116, 1.0 op_sel:[1,1,0]
	v_mfma_f32_16x16x32_f16 v[2:5], v[82:85], v[122:125], 0
	v_cvt_scalef32_pk_f16_fp4 v122, v117, 1.0
	v_cvt_scalef32_pk_f16_fp4 v123, v117, 1.0 op_sel:[1,0,0]
	v_cvt_scalef32_pk_f16_fp4 v124, v117, 1.0 op_sel:[0,1,0]
	v_cvt_scalef32_pk_f16_fp4 v125, v117, 1.0 op_sel:[1,1,0]
	v_mfma_f32_16x16x32_f16 v[6:9], v[82:85], v[126:129], 0
	v_cvt_scalef32_pk_f16_fp4 v126, v115, 1.0
	v_cvt_scalef32_pk_f16_fp4 v127, v115, 1.0 op_sel:[1,0,0]
	v_cvt_scalef32_pk_f16_fp4 v128, v115, 1.0 op_sel:[0,1,0]
	v_cvt_scalef32_pk_f16_fp4 v129, v115, 1.0 op_sel:[1,1,0]
	v_mfma_f32_16x16x32_f16 v[2:5], v[90:93], v[122:125], v[2:5]
	v_mfma_f32_16x16x32_f16 v[6:9], v[90:93], v[126:129], v[6:9]
	ds_read_b64_tr_b4 v[114:115], v152
	ds_read_b64_tr_b4 v[116:117], v160
	s_waitcnt lgkmcnt(2)
	v_cvt_scalef32_pk_f16_fp4 v122, v118, 1.0
	v_cvt_scalef32_pk_f16_fp4 v123, v118, 1.0 op_sel:[1,0,0]
	v_cvt_scalef32_pk_f16_fp4 v124, v118, 1.0 op_sel:[0,1,0]
	v_cvt_scalef32_pk_f16_fp4 v125, v118, 1.0 op_sel:[1,1,0]
	v_cvt_scalef32_pk_f16_fp4 v126, v120, 1.0
	v_cvt_scalef32_pk_f16_fp4 v127, v120, 1.0 op_sel:[1,0,0]
	v_cvt_scalef32_pk_f16_fp4 v128, v120, 1.0 op_sel:[0,1,0]
	v_cvt_scalef32_pk_f16_fp4 v129, v120, 1.0 op_sel:[1,1,0]
	v_mfma_f32_16x16x32_f16 v[10:13], v[82:85], v[122:125], 0
	v_cvt_scalef32_pk_f16_fp4 v122, v121, 1.0
	v_cvt_scalef32_pk_f16_fp4 v123, v121, 1.0 op_sel:[1,0,0]
	v_cvt_scalef32_pk_f16_fp4 v124, v121, 1.0 op_sel:[0,1,0]
	v_cvt_scalef32_pk_f16_fp4 v125, v121, 1.0 op_sel:[1,1,0]
	v_mfma_f32_16x16x32_f16 v[14:17], v[82:85], v[126:129], 0
	v_cvt_scalef32_pk_f16_fp4 v126, v119, 1.0
	v_cvt_scalef32_pk_f16_fp4 v127, v119, 1.0 op_sel:[1,0,0]
	v_cvt_scalef32_pk_f16_fp4 v128, v119, 1.0 op_sel:[0,1,0]
	v_cvt_scalef32_pk_f16_fp4 v129, v119, 1.0 op_sel:[1,1,0]
	v_mfma_f32_16x16x32_f16 v[10:13], v[90:93], v[122:125], v[10:13]
	v_mfma_f32_16x16x32_f16 v[14:17], v[90:93], v[126:129], v[14:17]
	ds_read_b64_tr_b4 v[118:119], v153
	ds_read_b64_tr_b4 v[120:121], v161
	s_waitcnt lgkmcnt(2)
	v_cvt_scalef32_pk_f16_fp4 v122, v114, 1.0
	v_cvt_scalef32_pk_f16_fp4 v123, v114, 1.0 op_sel:[1,0,0]
	v_cvt_scalef32_pk_f16_fp4 v124, v114, 1.0 op_sel:[0,1,0]
	v_cvt_scalef32_pk_f16_fp4 v125, v114, 1.0 op_sel:[1,1,0]
	v_cvt_scalef32_pk_f16_fp4 v126, v116, 1.0
	v_cvt_scalef32_pk_f16_fp4 v127, v116, 1.0 op_sel:[1,0,0]
	v_cvt_scalef32_pk_f16_fp4 v128, v116, 1.0 op_sel:[0,1,0]
	v_cvt_scalef32_pk_f16_fp4 v129, v116, 1.0 op_sel:[1,1,0]
	v_mfma_f32_16x16x32_f16 v[18:21], v[82:85], v[122:125], 0
	v_cvt_scalef32_pk_f16_fp4 v122, v117, 1.0
	v_cvt_scalef32_pk_f16_fp4 v123, v117, 1.0 op_sel:[1,0,0]
	v_cvt_scalef32_pk_f16_fp4 v124, v117, 1.0 op_sel:[0,1,0]
	v_cvt_scalef32_pk_f16_fp4 v125, v117, 1.0 op_sel:[1,1,0]
	v_mfma_f32_16x16x32_f16 v[22:25], v[82:85], v[126:129], 0
	v_cvt_scalef32_pk_f16_fp4 v126, v115, 1.0
	v_cvt_scalef32_pk_f16_fp4 v127, v115, 1.0 op_sel:[1,0,0]
	v_cvt_scalef32_pk_f16_fp4 v128, v115, 1.0 op_sel:[0,1,0]
	v_cvt_scalef32_pk_f16_fp4 v129, v115, 1.0 op_sel:[1,1,0]
	v_mfma_f32_16x16x32_f16 v[18:21], v[90:93], v[122:125], v[18:21]
	v_mfma_f32_16x16x32_f16 v[22:25], v[90:93], v[126:129], v[22:25]
	ds_read_b64_tr_b4 v[114:115], v154
	ds_read_b64_tr_b4 v[116:117], v162
	s_waitcnt lgkmcnt(2)
	v_cvt_scalef32_pk_f16_fp4 v122, v118, 1.0
	v_cvt_scalef32_pk_f16_fp4 v123, v118, 1.0 op_sel:[1,0,0]
	v_cvt_scalef32_pk_f16_fp4 v124, v118, 1.0 op_sel:[0,1,0]
	v_cvt_scalef32_pk_f16_fp4 v125, v118, 1.0 op_sel:[1,1,0]
	v_cvt_scalef32_pk_f16_fp4 v126, v120, 1.0
	v_cvt_scalef32_pk_f16_fp4 v127, v120, 1.0 op_sel:[1,0,0]
	v_cvt_scalef32_pk_f16_fp4 v128, v120, 1.0 op_sel:[0,1,0]
	v_cvt_scalef32_pk_f16_fp4 v129, v120, 1.0 op_sel:[1,1,0]
	v_mfma_f32_16x16x32_f16 v[26:29], v[82:85], v[122:125], 0
	v_cvt_scalef32_pk_f16_fp4 v122, v121, 1.0
	v_cvt_scalef32_pk_f16_fp4 v123, v121, 1.0 op_sel:[1,0,0]
	v_cvt_scalef32_pk_f16_fp4 v124, v121, 1.0 op_sel:[0,1,0]
	v_cvt_scalef32_pk_f16_fp4 v125, v121, 1.0 op_sel:[1,1,0]
	v_mfma_f32_16x16x32_f16 v[30:33], v[82:85], v[126:129], 0
	v_cvt_scalef32_pk_f16_fp4 v126, v119, 1.0
	v_cvt_scalef32_pk_f16_fp4 v127, v119, 1.0 op_sel:[1,0,0]
	v_cvt_scalef32_pk_f16_fp4 v128, v119, 1.0 op_sel:[0,1,0]
	v_cvt_scalef32_pk_f16_fp4 v129, v119, 1.0 op_sel:[1,1,0]
	v_mfma_f32_16x16x32_f16 v[26:29], v[90:93], v[122:125], v[26:29]
	v_mfma_f32_16x16x32_f16 v[30:33], v[90:93], v[126:129], v[30:33]
	ds_read_b64_tr_b4 v[118:119], v155
	ds_read_b64_tr_b4 v[120:121], v163
	s_waitcnt lgkmcnt(2)
	v_cvt_scalef32_pk_f16_fp4 v122, v114, 1.0
	v_cvt_scalef32_pk_f16_fp4 v123, v114, 1.0 op_sel:[1,0,0]
	v_cvt_scalef32_pk_f16_fp4 v124, v114, 1.0 op_sel:[0,1,0]
	v_cvt_scalef32_pk_f16_fp4 v125, v114, 1.0 op_sel:[1,1,0]
	v_cvt_scalef32_pk_f16_fp4 v126, v116, 1.0
	v_cvt_scalef32_pk_f16_fp4 v127, v116, 1.0 op_sel:[1,0,0]
	v_cvt_scalef32_pk_f16_fp4 v128, v116, 1.0 op_sel:[0,1,0]
	v_cvt_scalef32_pk_f16_fp4 v129, v116, 1.0 op_sel:[1,1,0]
	v_mfma_f32_16x16x32_f16 v[34:37], v[82:85], v[122:125], 0
	v_cvt_scalef32_pk_f16_fp4 v122, v117, 1.0
	v_cvt_scalef32_pk_f16_fp4 v123, v117, 1.0 op_sel:[1,0,0]
	v_cvt_scalef32_pk_f16_fp4 v124, v117, 1.0 op_sel:[0,1,0]
	v_cvt_scalef32_pk_f16_fp4 v125, v117, 1.0 op_sel:[1,1,0]
	v_mfma_f32_16x16x32_f16 v[38:41], v[82:85], v[126:129], 0
	v_cvt_scalef32_pk_f16_fp4 v126, v115, 1.0
	v_cvt_scalef32_pk_f16_fp4 v127, v115, 1.0 op_sel:[1,0,0]
	v_cvt_scalef32_pk_f16_fp4 v128, v115, 1.0 op_sel:[0,1,0]
	v_cvt_scalef32_pk_f16_fp4 v129, v115, 1.0 op_sel:[1,1,0]
	v_mfma_f32_16x16x32_f16 v[34:37], v[90:93], v[122:125], v[34:37]
	v_mfma_f32_16x16x32_f16 v[38:41], v[90:93], v[126:129], v[38:41]
	ds_read_b64_tr_b4 v[114:115], v156
	ds_read_b64_tr_b4 v[116:117], v164
	s_waitcnt lgkmcnt(2)
	v_cvt_scalef32_pk_f16_fp4 v122, v118, 1.0
	v_cvt_scalef32_pk_f16_fp4 v123, v118, 1.0 op_sel:[1,0,0]
	v_cvt_scalef32_pk_f16_fp4 v124, v118, 1.0 op_sel:[0,1,0]
	v_cvt_scalef32_pk_f16_fp4 v125, v118, 1.0 op_sel:[1,1,0]
	v_cvt_scalef32_pk_f16_fp4 v126, v120, 1.0
	v_cvt_scalef32_pk_f16_fp4 v127, v120, 1.0 op_sel:[1,0,0]
	v_cvt_scalef32_pk_f16_fp4 v128, v120, 1.0 op_sel:[0,1,0]
	v_cvt_scalef32_pk_f16_fp4 v129, v120, 1.0 op_sel:[1,1,0]
	v_mfma_f32_16x16x32_f16 v[42:45], v[82:85], v[122:125], 0
	v_cvt_scalef32_pk_f16_fp4 v122, v121, 1.0
	v_cvt_scalef32_pk_f16_fp4 v123, v121, 1.0 op_sel:[1,0,0]
	v_cvt_scalef32_pk_f16_fp4 v124, v121, 1.0 op_sel:[0,1,0]
	v_cvt_scalef32_pk_f16_fp4 v125, v121, 1.0 op_sel:[1,1,0]
	v_mfma_f32_16x16x32_f16 v[46:49], v[82:85], v[126:129], 0
	v_cvt_scalef32_pk_f16_fp4 v126, v119, 1.0
	v_cvt_scalef32_pk_f16_fp4 v127, v119, 1.0 op_sel:[1,0,0]
	v_cvt_scalef32_pk_f16_fp4 v128, v119, 1.0 op_sel:[0,1,0]
	v_cvt_scalef32_pk_f16_fp4 v129, v119, 1.0 op_sel:[1,1,0]
	v_mfma_f32_16x16x32_f16 v[42:45], v[90:93], v[122:125], v[42:45]
	v_mfma_f32_16x16x32_f16 v[46:49], v[90:93], v[126:129], v[46:49]
	ds_read_b64_tr_b4 v[118:119], v157
	ds_read_b64_tr_b4 v[120:121], v165
	s_waitcnt lgkmcnt(2)
	v_cvt_scalef32_pk_f16_fp4 v122, v114, 1.0
	v_cvt_scalef32_pk_f16_fp4 v123, v114, 1.0 op_sel:[1,0,0]
	v_cvt_scalef32_pk_f16_fp4 v124, v114, 1.0 op_sel:[0,1,0]
	v_cvt_scalef32_pk_f16_fp4 v125, v114, 1.0 op_sel:[1,1,0]
	v_cvt_scalef32_pk_f16_fp4 v126, v116, 1.0
	v_cvt_scalef32_pk_f16_fp4 v127, v116, 1.0 op_sel:[1,0,0]
	v_cvt_scalef32_pk_f16_fp4 v128, v116, 1.0 op_sel:[0,1,0]
	v_cvt_scalef32_pk_f16_fp4 v129, v116, 1.0 op_sel:[1,1,0]
	v_mfma_f32_16x16x32_f16 v[50:53], v[82:85], v[122:125], 0
	v_cvt_scalef32_pk_f16_fp4 v122, v117, 1.0
	v_cvt_scalef32_pk_f16_fp4 v123, v117, 1.0 op_sel:[1,0,0]
	v_cvt_scalef32_pk_f16_fp4 v124, v117, 1.0 op_sel:[0,1,0]
	v_cvt_scalef32_pk_f16_fp4 v125, v117, 1.0 op_sel:[1,1,0]
	v_mfma_f32_16x16x32_f16 v[54:57], v[82:85], v[126:129], 0
	v_cvt_scalef32_pk_f16_fp4 v126, v115, 1.0
	v_cvt_scalef32_pk_f16_fp4 v127, v115, 1.0 op_sel:[1,0,0]
	v_cvt_scalef32_pk_f16_fp4 v128, v115, 1.0 op_sel:[0,1,0]
	v_cvt_scalef32_pk_f16_fp4 v129, v115, 1.0 op_sel:[1,1,0]
	v_mfma_f32_16x16x32_f16 v[50:53], v[90:93], v[122:125], v[50:53]
	v_mfma_f32_16x16x32_f16 v[54:57], v[90:93], v[126:129], v[54:57]
	s_waitcnt vmcnt(10)
	ds_read_b64_tr_b4 v[114:115], v150 offset:8192
	ds_read_b64_tr_b4 v[116:117], v158 offset:8192
	s_waitcnt lgkmcnt(2)
	s_add_i32 m0, s38, 0x0
	v_mad_u32_u16 v178, v98, v198, v166
	global_load_lds_dwordx4 v178, s[40:41]
	s_add_i32 m0, s38, 0x400
	v_mad_u32_u16 v179, v98, v198, v167 op_sel:[1,0,0,0]
	global_load_lds_dwordx4 v179, s[40:41]
	s_add_i32 m0, s38, 0x800
	v_mad_u32_u16 v178, v99, v198, v168
	global_load_lds_dwordx4 v178, s[40:41]
	s_add_i32 m0, s38, 0xc00
	v_mad_u32_u16 v179, v99, v198, v169 op_sel:[1,0,0,0]
	global_load_lds_dwordx4 v179, s[40:41]
	s_add_i32 m0, s38, 0x1000
	v_mad_u32_u16 v178, v100, v198, v170
	global_load_lds_dwordx4 v178, s[40:41]
	s_add_i32 m0, s38, 0x1400
	v_mad_u32_u16 v179, v100, v198, v171 op_sel:[1,0,0,0]
	global_load_lds_dwordx4 v179, s[40:41]
	s_add_i32 m0, s38, 0x1800
	v_mad_u32_u16 v178, v101, v198, v172
	global_load_lds_dwordx4 v178, s[40:41]
	s_add_i32 m0, s38, 0x1c00
	v_mad_u32_u16 v179, v101, v198, v173 op_sel:[1,0,0,0]
	global_load_lds_dwordx4 v179, s[40:41]
	v_cvt_scalef32_pk_f16_fp4 v122, v118, 1.0
	v_cvt_scalef32_pk_f16_fp4 v123, v118, 1.0 op_sel:[1,0,0]
	v_cvt_scalef32_pk_f16_fp4 v124, v118, 1.0 op_sel:[0,1,0]
	v_cvt_scalef32_pk_f16_fp4 v125, v118, 1.0 op_sel:[1,1,0]
	v_cvt_scalef32_pk_f16_fp4 v126, v120, 1.0
	v_cvt_scalef32_pk_f16_fp4 v127, v120, 1.0 op_sel:[1,0,0]
	v_cvt_scalef32_pk_f16_fp4 v128, v120, 1.0 op_sel:[0,1,0]
	v_cvt_scalef32_pk_f16_fp4 v129, v120, 1.0 op_sel:[1,1,0]
	v_mfma_f32_16x16x32_f16 v[58:61], v[82:85], v[122:125], 0
	v_cvt_scalef32_pk_f16_fp4 v122, v121, 1.0
	v_cvt_scalef32_pk_f16_fp4 v123, v121, 1.0 op_sel:[1,0,0]
	v_cvt_scalef32_pk_f16_fp4 v124, v121, 1.0 op_sel:[0,1,0]
	v_cvt_scalef32_pk_f16_fp4 v125, v121, 1.0 op_sel:[1,1,0]
	v_mfma_f32_16x16x32_f16 v[62:65], v[82:85], v[126:129], 0
	v_cvt_scalef32_pk_f16_fp4 v126, v119, 1.0
	v_cvt_scalef32_pk_f16_fp4 v127, v119, 1.0 op_sel:[1,0,0]
	v_cvt_scalef32_pk_f16_fp4 v128, v119, 1.0 op_sel:[0,1,0]
	v_cvt_scalef32_pk_f16_fp4 v129, v119, 1.0 op_sel:[1,1,0]
	v_mfma_f32_16x16x32_f16 v[58:61], v[90:93], v[122:125], v[58:61]
	v_mfma_f32_16x16x32_f16 v[62:65], v[90:93], v[126:129], v[62:65]
	ds_read_b64_tr_b4 v[118:119], v151 offset:8192
	ds_read_b64_tr_b4 v[120:121], v159 offset:8192
	s_waitcnt lgkmcnt(2)
	v_cvt_scalef32_pk_f16_fp4 v122, v114, 1.0
	v_cvt_scalef32_pk_f16_fp4 v123, v114, 1.0 op_sel:[1,0,0]
	v_cvt_scalef32_pk_f16_fp4 v124, v114, 1.0 op_sel:[0,1,0]
	v_cvt_scalef32_pk_f16_fp4 v125, v114, 1.0 op_sel:[1,1,0]
	v_cvt_scalef32_pk_f16_fp4 v126, v116, 1.0
	v_cvt_scalef32_pk_f16_fp4 v127, v116, 1.0 op_sel:[1,0,0]
	v_cvt_scalef32_pk_f16_fp4 v128, v116, 1.0 op_sel:[0,1,0]
	v_cvt_scalef32_pk_f16_fp4 v129, v116, 1.0 op_sel:[1,1,0]
	v_mfma_f32_16x16x32_f16 v[2:5], v[86:89], v[122:125], v[2:5]
	v_cvt_scalef32_pk_f16_fp4 v122, v117, 1.0
	v_cvt_scalef32_pk_f16_fp4 v123, v117, 1.0 op_sel:[1,0,0]
	v_cvt_scalef32_pk_f16_fp4 v124, v117, 1.0 op_sel:[0,1,0]
	v_cvt_scalef32_pk_f16_fp4 v125, v117, 1.0 op_sel:[1,1,0]
	v_mfma_f32_16x16x32_f16 v[6:9], v[86:89], v[126:129], v[6:9]
	v_cvt_scalef32_pk_f16_fp4 v126, v115, 1.0
	v_cvt_scalef32_pk_f16_fp4 v127, v115, 1.0 op_sel:[1,0,0]
	v_cvt_scalef32_pk_f16_fp4 v128, v115, 1.0 op_sel:[0,1,0]
	v_cvt_scalef32_pk_f16_fp4 v129, v115, 1.0 op_sel:[1,1,0]
	v_mfma_f32_16x16x32_f16 v[2:5], v[94:97], v[122:125], v[2:5]
	v_mfma_f32_16x16x32_f16 v[6:9], v[94:97], v[126:129], v[6:9]
	ds_read_b64_tr_b4 v[114:115], v152 offset:8192
	ds_read_b64_tr_b4 v[116:117], v160 offset:8192
	s_waitcnt lgkmcnt(2)
	v_cvt_scalef32_pk_f16_fp4 v122, v118, 1.0
	v_cvt_scalef32_pk_f16_fp4 v123, v118, 1.0 op_sel:[1,0,0]
	v_cvt_scalef32_pk_f16_fp4 v124, v118, 1.0 op_sel:[0,1,0]
	v_cvt_scalef32_pk_f16_fp4 v125, v118, 1.0 op_sel:[1,1,0]
	v_cvt_scalef32_pk_f16_fp4 v126, v120, 1.0
	v_cvt_scalef32_pk_f16_fp4 v127, v120, 1.0 op_sel:[1,0,0]
	v_cvt_scalef32_pk_f16_fp4 v128, v120, 1.0 op_sel:[0,1,0]
	v_cvt_scalef32_pk_f16_fp4 v129, v120, 1.0 op_sel:[1,1,0]
	v_mfma_f32_16x16x32_f16 v[10:13], v[86:89], v[122:125], v[10:13]
	v_cvt_scalef32_pk_f16_fp4 v122, v121, 1.0
	v_cvt_scalef32_pk_f16_fp4 v123, v121, 1.0 op_sel:[1,0,0]
	v_cvt_scalef32_pk_f16_fp4 v124, v121, 1.0 op_sel:[0,1,0]
	v_cvt_scalef32_pk_f16_fp4 v125, v121, 1.0 op_sel:[1,1,0]
	v_mfma_f32_16x16x32_f16 v[14:17], v[86:89], v[126:129], v[14:17]
	v_cvt_scalef32_pk_f16_fp4 v126, v119, 1.0
	v_cvt_scalef32_pk_f16_fp4 v127, v119, 1.0 op_sel:[1,0,0]
	v_cvt_scalef32_pk_f16_fp4 v128, v119, 1.0 op_sel:[0,1,0]
	v_cvt_scalef32_pk_f16_fp4 v129, v119, 1.0 op_sel:[1,1,0]
	v_mfma_f32_16x16x32_f16 v[10:13], v[94:97], v[122:125], v[10:13]
	v_mfma_f32_16x16x32_f16 v[14:17], v[94:97], v[126:129], v[14:17]
	ds_read_b64_tr_b4 v[118:119], v153 offset:8192
	ds_read_b64_tr_b4 v[120:121], v161 offset:8192
	s_waitcnt lgkmcnt(2)
	v_cvt_scalef32_pk_f16_fp4 v122, v114, 1.0
	v_cvt_scalef32_pk_f16_fp4 v123, v114, 1.0 op_sel:[1,0,0]
	v_cvt_scalef32_pk_f16_fp4 v124, v114, 1.0 op_sel:[0,1,0]
	v_cvt_scalef32_pk_f16_fp4 v125, v114, 1.0 op_sel:[1,1,0]
	v_cvt_scalef32_pk_f16_fp4 v126, v116, 1.0
	v_cvt_scalef32_pk_f16_fp4 v127, v116, 1.0 op_sel:[1,0,0]
	v_cvt_scalef32_pk_f16_fp4 v128, v116, 1.0 op_sel:[0,1,0]
	v_cvt_scalef32_pk_f16_fp4 v129, v116, 1.0 op_sel:[1,1,0]
	v_mfma_f32_16x16x32_f16 v[18:21], v[86:89], v[122:125], v[18:21]
	v_cvt_scalef32_pk_f16_fp4 v122, v117, 1.0
	v_cvt_scalef32_pk_f16_fp4 v123, v117, 1.0 op_sel:[1,0,0]
	v_cvt_scalef32_pk_f16_fp4 v124, v117, 1.0 op_sel:[0,1,0]
	v_cvt_scalef32_pk_f16_fp4 v125, v117, 1.0 op_sel:[1,1,0]
	v_mfma_f32_16x16x32_f16 v[22:25], v[86:89], v[126:129], v[22:25]
	v_cvt_scalef32_pk_f16_fp4 v126, v115, 1.0
	v_cvt_scalef32_pk_f16_fp4 v127, v115, 1.0 op_sel:[1,0,0]
	v_cvt_scalef32_pk_f16_fp4 v128, v115, 1.0 op_sel:[0,1,0]
	v_cvt_scalef32_pk_f16_fp4 v129, v115, 1.0 op_sel:[1,1,0]
	v_mfma_f32_16x16x32_f16 v[18:21], v[94:97], v[122:125], v[18:21]
	v_mfma_f32_16x16x32_f16 v[22:25], v[94:97], v[126:129], v[22:25]
	ds_read_b64_tr_b4 v[114:115], v154 offset:8192
	ds_read_b64_tr_b4 v[116:117], v162 offset:8192
	s_waitcnt lgkmcnt(2)
	v_cvt_scalef32_pk_f16_fp4 v122, v118, 1.0
	v_cvt_scalef32_pk_f16_fp4 v123, v118, 1.0 op_sel:[1,0,0]
	v_cvt_scalef32_pk_f16_fp4 v124, v118, 1.0 op_sel:[0,1,0]
	v_cvt_scalef32_pk_f16_fp4 v125, v118, 1.0 op_sel:[1,1,0]
	v_cvt_scalef32_pk_f16_fp4 v126, v120, 1.0
	v_cvt_scalef32_pk_f16_fp4 v127, v120, 1.0 op_sel:[1,0,0]
	v_cvt_scalef32_pk_f16_fp4 v128, v120, 1.0 op_sel:[0,1,0]
	v_cvt_scalef32_pk_f16_fp4 v129, v120, 1.0 op_sel:[1,1,0]
	v_mfma_f32_16x16x32_f16 v[26:29], v[86:89], v[122:125], v[26:29]
	v_cvt_scalef32_pk_f16_fp4 v122, v121, 1.0
	v_cvt_scalef32_pk_f16_fp4 v123, v121, 1.0 op_sel:[1,0,0]
	v_cvt_scalef32_pk_f16_fp4 v124, v121, 1.0 op_sel:[0,1,0]
	v_cvt_scalef32_pk_f16_fp4 v125, v121, 1.0 op_sel:[1,1,0]
	v_mfma_f32_16x16x32_f16 v[30:33], v[86:89], v[126:129], v[30:33]
	v_cvt_scalef32_pk_f16_fp4 v126, v119, 1.0
	v_cvt_scalef32_pk_f16_fp4 v127, v119, 1.0 op_sel:[1,0,0]
	v_cvt_scalef32_pk_f16_fp4 v128, v119, 1.0 op_sel:[0,1,0]
	v_cvt_scalef32_pk_f16_fp4 v129, v119, 1.0 op_sel:[1,1,0]
	v_mfma_f32_16x16x32_f16 v[26:29], v[94:97], v[122:125], v[26:29]
	v_mfma_f32_16x16x32_f16 v[30:33], v[94:97], v[126:129], v[30:33]
	ds_read_b64_tr_b4 v[118:119], v155 offset:8192
	ds_read_b64_tr_b4 v[120:121], v163 offset:8192
	s_waitcnt lgkmcnt(2)
	v_cvt_scalef32_pk_f16_fp4 v122, v114, 1.0
	v_cvt_scalef32_pk_f16_fp4 v123, v114, 1.0 op_sel:[1,0,0]
	v_cvt_scalef32_pk_f16_fp4 v124, v114, 1.0 op_sel:[0,1,0]
	v_cvt_scalef32_pk_f16_fp4 v125, v114, 1.0 op_sel:[1,1,0]
	v_cvt_scalef32_pk_f16_fp4 v126, v116, 1.0
	v_cvt_scalef32_pk_f16_fp4 v127, v116, 1.0 op_sel:[1,0,0]
	v_cvt_scalef32_pk_f16_fp4 v128, v116, 1.0 op_sel:[0,1,0]
	v_cvt_scalef32_pk_f16_fp4 v129, v116, 1.0 op_sel:[1,1,0]
	v_mfma_f32_16x16x32_f16 v[34:37], v[86:89], v[122:125], v[34:37]
	v_cvt_scalef32_pk_f16_fp4 v122, v117, 1.0
	v_cvt_scalef32_pk_f16_fp4 v123, v117, 1.0 op_sel:[1,0,0]
	v_cvt_scalef32_pk_f16_fp4 v124, v117, 1.0 op_sel:[0,1,0]
	v_cvt_scalef32_pk_f16_fp4 v125, v117, 1.0 op_sel:[1,1,0]
	v_mfma_f32_16x16x32_f16 v[38:41], v[86:89], v[126:129], v[38:41]
	v_cvt_scalef32_pk_f16_fp4 v126, v115, 1.0
	v_cvt_scalef32_pk_f16_fp4 v127, v115, 1.0 op_sel:[1,0,0]
	v_cvt_scalef32_pk_f16_fp4 v128, v115, 1.0 op_sel:[0,1,0]
	v_cvt_scalef32_pk_f16_fp4 v129, v115, 1.0 op_sel:[1,1,0]
	v_mfma_f32_16x16x32_f16 v[34:37], v[94:97], v[122:125], v[34:37]
	v_mfma_f32_16x16x32_f16 v[38:41], v[94:97], v[126:129], v[38:41]
	ds_read_b64_tr_b4 v[114:115], v156 offset:8192
	ds_read_b64_tr_b4 v[116:117], v164 offset:8192
	s_waitcnt lgkmcnt(2)
	v_cvt_scalef32_pk_f16_fp4 v122, v118, 1.0
	v_cvt_scalef32_pk_f16_fp4 v123, v118, 1.0 op_sel:[1,0,0]
	v_cvt_scalef32_pk_f16_fp4 v124, v118, 1.0 op_sel:[0,1,0]
	v_cvt_scalef32_pk_f16_fp4 v125, v118, 1.0 op_sel:[1,1,0]
	v_cvt_scalef32_pk_f16_fp4 v126, v120, 1.0
	v_cvt_scalef32_pk_f16_fp4 v127, v120, 1.0 op_sel:[1,0,0]
	v_cvt_scalef32_pk_f16_fp4 v128, v120, 1.0 op_sel:[0,1,0]
	v_cvt_scalef32_pk_f16_fp4 v129, v120, 1.0 op_sel:[1,1,0]
	v_mfma_f32_16x16x32_f16 v[42:45], v[86:89], v[122:125], v[42:45]
	v_cvt_scalef32_pk_f16_fp4 v122, v121, 1.0
	v_cvt_scalef32_pk_f16_fp4 v123, v121, 1.0 op_sel:[1,0,0]
	v_cvt_scalef32_pk_f16_fp4 v124, v121, 1.0 op_sel:[0,1,0]
	v_cvt_scalef32_pk_f16_fp4 v125, v121, 1.0 op_sel:[1,1,0]
	v_mfma_f32_16x16x32_f16 v[46:49], v[86:89], v[126:129], v[46:49]
	v_cvt_scalef32_pk_f16_fp4 v126, v119, 1.0
	v_cvt_scalef32_pk_f16_fp4 v127, v119, 1.0 op_sel:[1,0,0]
	v_cvt_scalef32_pk_f16_fp4 v128, v119, 1.0 op_sel:[0,1,0]
	v_cvt_scalef32_pk_f16_fp4 v129, v119, 1.0 op_sel:[1,1,0]
	v_mfma_f32_16x16x32_f16 v[42:45], v[94:97], v[122:125], v[42:45]
	v_mfma_f32_16x16x32_f16 v[46:49], v[94:97], v[126:129], v[46:49]
	ds_read_b64_tr_b4 v[118:119], v157 offset:8192
	ds_read_b64_tr_b4 v[120:121], v165 offset:8192
	s_waitcnt lgkmcnt(2)
	v_cvt_scalef32_pk_f16_fp4 v122, v114, 1.0
	v_cvt_scalef32_pk_f16_fp4 v123, v114, 1.0 op_sel:[1,0,0]
	v_cvt_scalef32_pk_f16_fp4 v124, v114, 1.0 op_sel:[0,1,0]
	v_cvt_scalef32_pk_f16_fp4 v125, v114, 1.0 op_sel:[1,1,0]
	v_cvt_scalef32_pk_f16_fp4 v126, v116, 1.0
	v_cvt_scalef32_pk_f16_fp4 v127, v116, 1.0 op_sel:[1,0,0]
	v_cvt_scalef32_pk_f16_fp4 v128, v116, 1.0 op_sel:[0,1,0]
	v_cvt_scalef32_pk_f16_fp4 v129, v116, 1.0 op_sel:[1,1,0]
	v_mfma_f32_16x16x32_f16 v[50:53], v[86:89], v[122:125], v[50:53]
	v_cvt_scalef32_pk_f16_fp4 v122, v117, 1.0
	v_cvt_scalef32_pk_f16_fp4 v123, v117, 1.0 op_sel:[1,0,0]
	v_cvt_scalef32_pk_f16_fp4 v124, v117, 1.0 op_sel:[0,1,0]
	v_cvt_scalef32_pk_f16_fp4 v125, v117, 1.0 op_sel:[1,1,0]
	v_mfma_f32_16x16x32_f16 v[54:57], v[86:89], v[126:129], v[54:57]
	v_cvt_scalef32_pk_f16_fp4 v126, v115, 1.0
	v_cvt_scalef32_pk_f16_fp4 v127, v115, 1.0 op_sel:[1,0,0]
	v_cvt_scalef32_pk_f16_fp4 v128, v115, 1.0 op_sel:[0,1,0]
	v_cvt_scalef32_pk_f16_fp4 v129, v115, 1.0 op_sel:[1,1,0]
	v_mfma_f32_16x16x32_f16 v[50:53], v[94:97], v[122:125], v[50:53]
	v_mfma_f32_16x16x32_f16 v[54:57], v[94:97], v[126:129], v[54:57]
	s_waitcnt vmcnt(0)
	ds_read_b64_tr_b4 v[114:115], v150
	ds_read_b64_tr_b4 v[116:117], v158
	s_waitcnt lgkmcnt(2)
	s_add_i32 m0, s38, 0x2000
	v_mad_u32_u16 v178, v102, v198, v166
	global_load_lds_dwordx4 v178, s[40:41]
	s_add_i32 m0, s38, 0x2400
	v_mad_u32_u16 v179, v102, v198, v167 op_sel:[1,0,0,0]
	global_load_lds_dwordx4 v179, s[40:41]
	s_add_i32 m0, s38, 0x2800
	v_mad_u32_u16 v178, v103, v198, v168
	global_load_lds_dwordx4 v178, s[40:41]
	s_add_i32 m0, s38, 0x2c00
	v_mad_u32_u16 v179, v103, v198, v169 op_sel:[1,0,0,0]
	global_load_lds_dwordx4 v179, s[40:41]
	s_add_i32 m0, s38, 0x3000
	v_mad_u32_u16 v178, v104, v198, v170
	global_load_lds_dwordx4 v178, s[40:41]
	s_add_i32 m0, s38, 0x3400
	v_mad_u32_u16 v179, v104, v198, v171 op_sel:[1,0,0,0]
	global_load_lds_dwordx4 v179, s[40:41]
	s_add_i32 m0, s38, 0x3800
	v_mad_u32_u16 v178, v105, v198, v172
	global_load_lds_dwordx4 v178, s[40:41]
	s_add_i32 m0, s38, 0x3c00
	v_mad_u32_u16 v179, v105, v198, v173 op_sel:[1,0,0,0]
	global_load_lds_dwordx4 v179, s[40:41]
	ds_read_b128 v[66:69], v174
	ds_read_b128 v[70:73], v174 offset:16
	ds_read_b128 v[74:77], v175
	ds_read_b128 v[78:81], v175 offset:16
	ds_read_b128 v[106:109], v199 offset:256
	ds_read_b128 v[110:113], v199 offset:272
	v_cvt_scalef32_pk_f16_fp4 v122, v118, 1.0
	v_cvt_scalef32_pk_f16_fp4 v123, v118, 1.0 op_sel:[1,0,0]
	v_cvt_scalef32_pk_f16_fp4 v124, v118, 1.0 op_sel:[0,1,0]
	v_cvt_scalef32_pk_f16_fp4 v125, v118, 1.0 op_sel:[1,1,0]
	v_cvt_scalef32_pk_f16_fp4 v126, v120, 1.0
	v_cvt_scalef32_pk_f16_fp4 v127, v120, 1.0 op_sel:[1,0,0]
	v_cvt_scalef32_pk_f16_fp4 v128, v120, 1.0 op_sel:[0,1,0]
	v_cvt_scalef32_pk_f16_fp4 v129, v120, 1.0 op_sel:[1,1,0]
	v_mfma_f32_16x16x32_f16 v[58:61], v[86:89], v[122:125], v[58:61]
	v_cvt_scalef32_pk_f16_fp4 v122, v121, 1.0
	v_cvt_scalef32_pk_f16_fp4 v123, v121, 1.0 op_sel:[1,0,0]
	v_cvt_scalef32_pk_f16_fp4 v124, v121, 1.0 op_sel:[0,1,0]
	v_cvt_scalef32_pk_f16_fp4 v125, v121, 1.0 op_sel:[1,1,0]
	v_mfma_f32_16x16x32_f16 v[62:65], v[86:89], v[126:129], v[62:65]
	v_cvt_scalef32_pk_f16_fp4 v126, v119, 1.0
	v_cvt_scalef32_pk_f16_fp4 v127, v119, 1.0 op_sel:[1,0,0]
	v_cvt_scalef32_pk_f16_fp4 v128, v119, 1.0 op_sel:[0,1,0]
	v_cvt_scalef32_pk_f16_fp4 v129, v119, 1.0 op_sel:[1,1,0]
	v_mfma_f32_16x16x32_f16 v[58:61], v[94:97], v[122:125], v[58:61]
	v_mfma_f32_16x16x32_f16 v[62:65], v[94:97], v[126:129], v[62:65]
	s_nop 7
	s_nop 7
	v_cmp_ne_u32_e32 vcc, 0, v196
	v_cndmask_b32_e32 v146, v2, v6, vcc
	v_cndmask_b32_e32 v142, v10, v14, vcc
	v_cndmask_b32_e32 v147, v18, v22, vcc
	v_cndmask_b32_e32 v143, v26, v30, vcc
	v_cndmask_b32_e32 v148, v34, v38, vcc
	v_cndmask_b32_e32 v144, v42, v46, vcc
	v_cndmask_b32_e32 v149, v50, v54, vcc
	v_cndmask_b32_e32 v145, v58, v62, vcc
	v_cmp_ne_u32_e32 vcc, 0, v197
	v_cndmask_b32_e32 v146, v146, v142, vcc
	v_cndmask_b32_e32 v147, v147, v143, vcc
	v_cndmask_b32_e32 v148, v148, v144, vcc
	v_cndmask_b32_e32 v149, v149, v145, vcc
	v_fma_f32 v142, v134, v146, v130
	v_fma_f32 v143, v135, v147, v131
	v_fma_f32 v144, v136, v148, v132
	v_fma_f32 v145, v137, v149, v133
	global_store_dword v[180:181], v142, off
	global_store_dword v[180:181], v143, off offset:256
	global_store_dword v[180:181], v144, off offset:512
	global_store_dword v[180:181], v145, off offset:768
	v_lshl_add_u64 v[180:181], v[180:181], 0, s[48:49]
	s_add_i32 s33, s33, 2
	s_cmp_lt_u32 s33, 8
	s_cbranch_scc1 .Le2_loop
	s_cmp_lt_i32 s35, 0
	s_cbranch_scc1 .Le2_exit
	s_add_i32 s39, s39, s43
	s_add_i32 s39, s39, 7
	v_mov_b32_e32 v180, v182
	v_mov_b32_e32 v181, v183
	v_mov_b32_e32 v134, v138
	v_mov_b32_e32 v135, v139
	v_mov_b32_e32 v136, v140
	v_mov_b32_e32 v137, v141
	s_mov_b32 s33, 0
	s_branch .Le2_loop
